# P7: LayerNorm gamma/beta hoisted into registers once per phase (removes 4 serialized global loads + vmcnt(0) per row); counted waits per row
# speedup vs baseline: 1.0084x; 1.0084x over previous
; #define GAS __attribute__((address_space(1)))
; __device__ __forceinline__ const GAS float* inp(const Frame& F, int i) { return (const GAS float*)*(const float* const __attribute__((address_space(4)))*)(F.ka + 8 * i); }
; __device__ __forceinline__ void ln_row(f32x4 (&v)[4], const GAS float* g, const GAS float* b, int lane) {
;     ...
;     for (int j = 0; j < 4; ++j) { const f32x4 gg = *(const GAS f32x4*)(g + 4 * lane + 256 * j), bb = *(const GAS f32x4*)(b + 4 * lane + 256 * j); v[j] = v[j] * rstd * gg + bb; }
; __device__ __forceinline__ void p7_combine(Frame& F, int l) {
;     const int gw = F.vcu * NWAVES + F.wave, NGW = F.G * NWAVES, lane = F.lane;
;     const GAS unsigned char* y4 = (const GAS unsigned char*)(F.ws + WS_Y4);
;     GAS signed char* HQ = (GAS signed char*)(F.ws + WS_HB); GAS float* HS = (GAS float*)(F.ws + WS_HS);
;     const GAS float* g2 = inp(F, 19) + l * D; const GAS float* b2 = inp(F, 20) + l * D;
;     const bool lastl = (l == DEPTH - 1);
;     for (int m = 4 * gw; m < M; m += 4 * NGW) {
.LBB0_1051:
	s_or_b64 exec, exec, s[4:5]
	s_waitcnt lgkmcnt(0)
	v_mov_b32_e32 v0, s12
	v_mov_b32_e32 v1, s13
	s_barrier
	v_readlane_b32 s4, v253, 48
	v_readfirstlane_b32 s40, v0
	v_readfirstlane_b32 s41, v1
	v_mov_b32_e32 v0, s27
	v_mov_b32_e32 v1, s29
	v_readlane_b32 s5, v253, 49
	v_readfirstlane_b32 s42, v0
	v_readfirstlane_b32 s43, v1
	v_mov_b32_e32 v0, s17
	v_mov_b32_e32 v1, s25
	v_mov_b32_e32 v39, v179
	v_readfirstlane_b32 s44, v0
	v_readfirstlane_b32 s45, v1
	s_andn2_b64 vcc, exec, s[4:5]
	s_cbranch_vccnz .LBB0_1078
	s_load_dwordx4 s[12:15], s[40:41], 0x98
	v_readlane_b32 s4, v255, 8
	s_lshl_b32 s92, s4, 10
	s_lshl_b64 s[4:5], s[92:93], 2
	v_and_b32_e32 v2, 63, v39
	s_waitcnt lgkmcnt(0)
	s_add_u32 s10, s14, s4
	s_addc_u32 s11, s15, s5
	v_lshlrev_b32_e32 v168, 2, v2
	s_add_u32 s4, s12, s4
	s_addc_u32 s5, s13, s5
	v_lshl_add_u64 v[0:1], s[42:43], 0, v[168:169]
	s_mov_b64 s[12:13], 0x4d400000
	v_lshl_add_u64 v[24:25], v[0:1], 0, s[12:13]
	v_lshlrev_b32_e32 v0, 4, v2
	v_mov_b32_e32 v1, v169
	v_lshl_add_u64 v[26:27], s[4:5], 0, v[0:1]
	v_readlane_b32 s4, v254, 18
	v_readlane_b32 s5, v254, 19
	s_add_u32 s4, s42, s4
	s_addc_u32 s5, s43, s5
	s_add_u32 s4, s4, 0x1d400000
	v_lshl_add_u64 v[28:29], s[10:11], 0, v[0:1]
	s_addc_u32 s5, s5, 0
	v_readlane_b32 s10, v254, 20
	v_readlane_b32 s11, v254, 21
	s_add_u32 s10, s42, s10
	s_addc_u32 s11, s43, s11
	v_lshl_add_u64 v[30:31], s[44:45], 0, v[0:1]
	v_lshl_add_u64 v[0:1], s[10:11], 0, v[168:169]
	s_mov_b64 s[10:11], 0x19400000
	v_lshl_add_u64 v[32:33], v[0:1], 0, s[10:11]
	v_readlane_b32 s10, v254, 48
	v_cmp_eq_u32_e64 s[34:35], 0, v2
	s_mov_b32 s12, s10
	v_readlane_b32 s11, v254, 49
	global_load_dwordx4 v[204:207], v[26:27], off
	global_load_dwordx4 v[208:211], v[26:27], off offset:1024
	global_load_dwordx4 v[212:215], v[26:27], off offset:2048
	global_load_dwordx4 v[216:219], v[26:27], off offset:3072
	global_load_dwordx4 v[220:223], v[28:29], off
	global_load_dwordx4 v[224:227], v[28:29], off offset:1024
	global_load_dwordx4 v[228:231], v[28:29], off offset:2048
	global_load_dwordx4 v[232:235], v[28:29], off offset:3072
	s_waitcnt vmcnt(0)
	s_branch .LBB0_1055

; #define GAS __attribute__((address_space(1)))
; __device__ __forceinline__ void p7_combine(Frame& F, int l) {
;     ...
;         f32x4 v[4][4]; unsigned hv[4][4]; float hsa[4]; unsigned yv[4][4][4];
; #pragma unroll
;         for (int r = 0; r < 4; ++r) {
; #pragma unroll
;             for (int j = 0; j < 4; ++j) hv[r][j] = *(const GAS unsigned*)(HQ + (size_t)(m + r) * D + 4 * lane + 256 * j);
;             hsa[r] = HS[m + r] * ALPHA;
; #pragma unroll
;             for (int k = 0; k < 4; ++k)
; #pragma unroll
;                 for (int j = 0; j < 4; ++j) yv[r][k][j] = *(const GAS unsigned*)(y4 + ((size_t)(m + r) * 4 + k) * D + 4 * lane + 256 * j); }
.LBB0_1055:
	v_readlane_b32 s14, v254, 50
	v_readlane_b32 s15, v254, 51
	global_load_dword v6, v[32:33], off offset:-3840
	global_load_dword v8, v[32:33], off offset:-3584
	global_load_dword v12, v[32:33], off offset:-3328
	global_load_dword v16, v[32:33], off offset:-3072
	global_load_dwordx4 v[0:3], v169, s[4:5] offset:-8
	v_lshl_add_u64 v[4:5], v[24:25], 0, s[14:15]
	global_load_dword v7, v[4:5], off
	global_load_dword v9, v[4:5], off offset:256
	global_load_dword v13, v[4:5], off offset:512
	global_load_dword v17, v[4:5], off offset:768
	global_load_dword v23, v[4:5], off offset:1024
	global_load_dword v10, v[4:5], off offset:1280
	global_load_dword v14, v[4:5], off offset:1536
	global_load_dword v18, v[4:5], off offset:1792
	global_load_dword v34, v[4:5], off offset:2048
	global_load_dword v11, v[4:5], off offset:2304
	global_load_dword v15, v[4:5], off offset:2560
	global_load_dword v19, v[4:5], off offset:2816
	global_load_dword v35, v[4:5], off offset:3072
	global_load_dword v22, v[4:5], off offset:3328
	global_load_dword v21, v[4:5], off offset:3584
	global_load_dword v20, v[4:5], off offset:3840
	global_load_dword v94, v[32:33], off offset:-2816
	global_load_dword v89, v[32:33], off offset:-2560
	global_load_dword v84, v[32:33], off offset:-2304
	global_load_dword v38, v[32:33], off offset:-2048
	v_add_co_u32_e32 v36, vcc, s39, v4
	s_movk_i32 s10, 0x2000
	s_nop 0
	v_addc_co_u32_e32 v37, vcc, 0, v5, vcc
	v_add_co_u32_e32 v40, vcc, s10, v4
	s_movk_i32 s10, 0x3000
	s_nop 0
	v_addc_co_u32_e32 v41, vcc, 0, v5, vcc
	global_load_dword v95, v[40:41], off offset:-4096
	global_load_dword v90, v[36:37], off offset:256
	global_load_dword v85, v[36:37], off offset:512
	global_load_dword v80, v[36:37], off offset:768
	global_load_dword v96, v[36:37], off offset:1024
	global_load_dword v91, v[36:37], off offset:1280
	global_load_dword v86, v[36:37], off offset:1536
	global_load_dword v81, v[36:37], off offset:1792
	global_load_dword v97, v[36:37], off offset:2048
	global_load_dword v92, v[36:37], off offset:2304
	global_load_dword v87, v[36:37], off offset:2560
	global_load_dword v82, v[36:37], off offset:2816
	global_load_dword v98, v[36:37], off offset:3072
	global_load_dword v93, v[36:37], off offset:3328
	global_load_dword v88, v[36:37], off offset:3584
	global_load_dword v83, v[36:37], off offset:3840
	global_load_dword v75, v[32:33], off offset:-1792
	global_load_dword v70, v[32:33], off offset:-1536
	global_load_dword v65, v[32:33], off offset:-1280
	global_load_dword v60, v[32:33], off offset:-1024
	global_load_dword v76, v[40:41], off
	global_load_dword v71, v[40:41], off offset:256
	global_load_dword v66, v[40:41], off offset:512
	global_load_dword v61, v[40:41], off offset:768
	global_load_dword v77, v[40:41], off offset:1024
	global_load_dword v72, v[40:41], off offset:1280
	global_load_dword v67, v[40:41], off offset:1536
	global_load_dword v62, v[40:41], off offset:1792
	global_load_dword v78, v[40:41], off offset:2048
	global_load_dword v73, v[40:41], off offset:2304
	global_load_dword v68, v[40:41], off offset:2560
	global_load_dword v63, v[40:41], off offset:2816
	global_load_dword v79, v[40:41], off offset:3072
	global_load_dword v74, v[40:41], off offset:3328
	global_load_dword v69, v[40:41], off offset:3584
	global_load_dword v64, v[40:41], off offset:3840
	global_load_dword v43, v[32:33], off offset:-768
	global_load_dword v42, v[32:33], off offset:-512
	s_nop 0
	global_load_dword v41, v[32:33], off offset:-256
	global_load_dword v40, v[32:33], off
	v_add_co_u32_e32 v4, vcc, s10, v4
	s_mov_b32 s10, 0x3d800000
	s_nop 0
	v_addc_co_u32_e32 v5, vcc, 0, v5, vcc
	global_load_dword v56, v[4:5], off
	global_load_dword v52, v[4:5], off offset:256
	global_load_dword v48, v[4:5], off offset:512
	global_load_dword v44, v[4:5], off offset:768
	global_load_dword v57, v[4:5], off offset:1024
	global_load_dword v53, v[4:5], off offset:1280
	global_load_dword v49, v[4:5], off offset:1536
	global_load_dword v45, v[4:5], off offset:1792
	global_load_dword v58, v[4:5], off offset:2048
	global_load_dword v54, v[4:5], off offset:2304
	global_load_dword v50, v[4:5], off offset:2560
	global_load_dword v46, v[4:5], off offset:2816
	global_load_dword v59, v[4:5], off offset:3072
	global_load_dword v55, v[4:5], off offset:3328
	global_load_dword v51, v[4:5], off offset:3584
	global_load_dword v47, v[4:5], off offset:3840
	v_readlane_b32 s22, v255, 10
	v_readlane_b32 s23, v255, 11
	s_andn2_b64 vcc, exec, s[22:23]
	s_waitcnt vmcnt(62)
; __device__ __forceinline__ void p7_combine(Frame& F, int l) {
;     ...
;         for (int r = 0; r < 4; ++r) {
; #pragma unroll
;             for (int j = 0; j < 4; ++j) { const int hw = (int)hv[r][j]; f32x4 a; a.x = (float)((hw << 24) >> 24) * hsa[r]; a.y = (float)((hw << 16) >> 24) * hsa[r]; a.z = (float)((hw << 8) >> 24) * hsa[r]; a.w = (float)(hw >> 24) * hsa[r];
;                 f32x4 ys = (f32x4){0.f, 0.f, 0.f, 0.f};
; #pragma unroll
;                 for (int k = 0; k < 4; ++k) { const int w = (int)yv[r][k][j]; ys.x += __builtin_amdgcn_cvt_f32_fp8(w, 0); ys.y += __builtin_amdgcn_cvt_f32_fp8(w, 1); ys.z += __builtin_amdgcn_cvt_f32_fp8(w, 2); ys.w += __builtin_amdgcn_cvt_f32_fp8(w, 3); }
;                 v[r][j] = a + ys * (1.0f / 16.0f); }
	v_cvt_f32_fp8_sdwa v36, v7 src0_sel:BYTE_2
	v_cvt_f32_fp8_sdwa v37, v7 src0_sel:BYTE_3
	v_cvt_f32_fp8_e32 v4, v7
	v_cvt_f32_fp8_sdwa v5, v7 src0_sel:BYTE_1
	v_cvt_f32_fp8_sdwa v102, v23 src0_sel:BYTE_2
	v_cvt_f32_fp8_sdwa v103, v23 src0_sel:BYTE_3
	v_cvt_f32_fp8_e32 v100, v23
	v_cvt_f32_fp8_sdwa v101, v23 src0_sel:BYTE_1
	v_cvt_f32_fp8_sdwa v106, v34 src0_sel:BYTE_2
	v_cvt_f32_fp8_sdwa v107, v34 src0_sel:BYTE_3
	v_cvt_f32_fp8_e32 v104, v34
	v_cvt_f32_fp8_sdwa v105, v34 src0_sel:BYTE_1
	v_cvt_f32_fp8_e32 v108, v35
	v_cvt_f32_fp8_sdwa v109, v35 src0_sel:BYTE_1
	v_cvt_f32_fp8_sdwa v34, v35 src0_sel:BYTE_2
	v_cvt_f32_fp8_sdwa v35, v35 src0_sel:BYTE_3
	v_pk_add_f32 v[36:37], v[36:37], 0 op_sel_hi:[1,0]
	v_pk_add_f32 v[4:5], v[4:5], 0 op_sel_hi:[1,0]
	v_pk_add_f32 v[36:37], v[36:37], v[102:103]
	v_pk_add_f32 v[4:5], v[4:5], v[100:101]
	v_pk_add_f32 v[36:37], v[36:37], v[106:107]
	v_cvt_f32_i32_sdwa v7, sext(v6) dst_sel:DWORD dst_unused:UNUSED_PAD src0_sel:BYTE_3
	v_pk_add_f32 v[34:35], v[36:37], v[34:35]
	v_cvt_f32_i32_sdwa v37, sext(v6) dst_sel:DWORD dst_unused:UNUSED_PAD src0_sel:BYTE_1
	v_cvt_f32_i32_sdwa v36, sext(v6) dst_sel:DWORD dst_unused:UNUSED_PAD src0_sel:BYTE_0
	v_cvt_f32_i32_sdwa v6, sext(v6) dst_sel:DWORD dst_unused:UNUSED_PAD src0_sel:BYTE_2
	v_pk_add_f32 v[4:5], v[4:5], v[104:105]
	v_mul_f32_e32 v0, 0x3fb504f3, v0
	v_pk_add_f32 v[4:5], v[4:5], v[108:109]
	v_cvt_f32_fp8_sdwa v102, v10 src0_sel:BYTE_2
	v_pk_mul_f32 v[100:101], v[4:5], s[10:11] op_sel_hi:[1,0]
	v_pk_mul_f32 v[4:5], v[34:35], s[10:11] op_sel_hi:[1,0]
	v_cvt_f32_fp8_e32 v34, v9
	v_pk_fma_f32 v[4:5], v[0:1], v[6:7], v[4:5] op_sel_hi:[0,1,1]
	v_pk_fma_f32 v[6:7], v[0:1], v[36:37], v[100:101] op_sel_hi:[0,1,1]
	v_cvt_f32_fp8_sdwa v35, v9 src0_sel:BYTE_1
	v_cvt_f32_fp8_sdwa v36, v9 src0_sel:BYTE_2
	v_cvt_f32_fp8_sdwa v37, v9 src0_sel:BYTE_3
	v_cvt_f32_fp8_sdwa v103, v10 src0_sel:BYTE_3
	v_cvt_f32_fp8_e32 v100, v10
	v_cvt_f32_fp8_sdwa v101, v10 src0_sel:BYTE_1
	v_cvt_f32_fp8_e32 v104, v11
	v_cvt_f32_fp8_sdwa v105, v11 src0_sel:BYTE_1
	v_cvt_f32_fp8_sdwa v10, v11 src0_sel:BYTE_2
	v_cvt_f32_fp8_sdwa v11, v11 src0_sel:BYTE_3
	v_cvt_f32_fp8_e32 v106, v22
	v_cvt_f32_fp8_sdwa v107, v22 src0_sel:BYTE_1
	v_cvt_f32_fp8_sdwa v108, v22 src0_sel:BYTE_2
	v_cvt_f32_fp8_sdwa v109, v22 src0_sel:BYTE_3
	v_pk_add_f32 v[22:23], v[34:35], 0 op_sel_hi:[1,0]
	v_pk_add_f32 v[34:35], v[36:37], 0 op_sel_hi:[1,0]
	v_pk_add_f32 v[22:23], v[22:23], v[100:101]
	v_pk_add_f32 v[34:35], v[34:35], v[102:103]
	v_cvt_f32_i32_sdwa v9, sext(v8) dst_sel:DWORD dst_unused:UNUSED_PAD src0_sel:BYTE_3
	v_pk_add_f32 v[10:11], v[34:35], v[10:11]
	v_cvt_f32_i32_sdwa v35, sext(v8) dst_sel:DWORD dst_unused:UNUSED_PAD src0_sel:BYTE_1
	v_cvt_f32_i32_sdwa v34, sext(v8) dst_sel:DWORD dst_unused:UNUSED_PAD src0_sel:BYTE_0
	v_cvt_f32_i32_sdwa v8, sext(v8) dst_sel:DWORD dst_unused:UNUSED_PAD src0_sel:BYTE_2
	v_pk_add_f32 v[22:23], v[22:23], v[104:105]
	v_pk_add_f32 v[10:11], v[10:11], v[108:109]
	v_pk_add_f32 v[22:23], v[22:23], v[106:107]
	v_pk_mul_f32 v[10:11], v[10:11], s[10:11] op_sel_hi:[1,0]
	v_pk_mul_f32 v[22:23], v[22:23], s[10:11] op_sel_hi:[1,0]
	v_pk_fma_f32 v[8:9], v[0:1], v[8:9], v[10:11] op_sel_hi:[0,1,1]
	v_pk_fma_f32 v[10:11], v[0:1], v[34:35], v[22:23] op_sel_hi:[0,1,1]
	v_cvt_f32_fp8_sdwa v34, v13 src0_sel:BYTE_2
	v_cvt_f32_fp8_sdwa v35, v13 src0_sel:BYTE_3
	v_cvt_f32_fp8_e32 v22, v13
	v_cvt_f32_fp8_sdwa v23, v13 src0_sel:BYTE_1
	v_cvt_f32_fp8_sdwa v100, v14 src0_sel:BYTE_2
	v_cvt_f32_fp8_sdwa v101, v14 src0_sel:BYTE_3
	v_cvt_f32_fp8_e32 v36, v14
	v_cvt_f32_fp8_sdwa v37, v14 src0_sel:BYTE_1
	v_cvt_f32_fp8_e32 v102, v15
	v_cvt_f32_fp8_sdwa v103, v15 src0_sel:BYTE_1
	v_cvt_f32_fp8_sdwa v14, v15 src0_sel:BYTE_2
	v_cvt_f32_fp8_sdwa v15, v15 src0_sel:BYTE_3
	s_waitcnt vmcnt(61)
	v_cvt_f32_fp8_e32 v104, v21
	v_cvt_f32_fp8_sdwa v105, v21 src0_sel:BYTE_1
	v_cvt_f32_fp8_sdwa v106, v21 src0_sel:BYTE_2
	v_cvt_f32_fp8_sdwa v107, v21 src0_sel:BYTE_3
	v_pk_add_f32 v[34:35], v[34:35], 0 op_sel_hi:[1,0]
	v_pk_add_f32 v[22:23], v[22:23], 0 op_sel_hi:[1,0]
	v_pk_add_f32 v[34:35], v[34:35], v[100:101]
	v_pk_add_f32 v[22:23], v[22:23], v[36:37]
	v_pk_add_f32 v[14:15], v[34:35], v[14:15]
	v_cvt_f32_i32_sdwa v13, sext(v12) dst_sel:DWORD dst_unused:UNUSED_PAD src0_sel:BYTE_3
	v_cvt_f32_i32_sdwa v35, sext(v12) dst_sel:DWORD dst_unused:UNUSED_PAD src0_sel:BYTE_1
	v_cvt_f32_i32_sdwa v34, sext(v12) dst_sel:DWORD dst_unused:UNUSED_PAD src0_sel:BYTE_0
	v_cvt_f32_i32_sdwa v12, sext(v12) dst_sel:DWORD dst_unused:UNUSED_PAD src0_sel:BYTE_2
	v_pk_add_f32 v[22:23], v[22:23], v[102:103]
	v_pk_add_f32 v[14:15], v[14:15], v[106:107]
	v_pk_add_f32 v[22:23], v[22:23], v[104:105]
	v_pk_mul_f32 v[14:15], v[14:15], s[10:11] op_sel_hi:[1,0]
	v_pk_mul_f32 v[22:23], v[22:23], s[10:11] op_sel_hi:[1,0]
	v_pk_fma_f32 v[12:13], v[0:1], v[12:13], v[14:15] op_sel_hi:[0,1,1]
	v_pk_fma_f32 v[14:15], v[0:1], v[34:35], v[22:23] op_sel_hi:[0,1,1]
	v_cvt_f32_fp8_e32 v22, v17
	v_cvt_f32_fp8_sdwa v23, v17 src0_sel:BYTE_1
	v_cvt_f32_fp8_sdwa v34, v17 src0_sel:BYTE_2
	v_cvt_f32_fp8_sdwa v35, v17 src0_sel:BYTE_3
	v_cvt_f32_fp8_sdwa v100, v18 src0_sel:BYTE_2
	v_cvt_f32_fp8_sdwa v101, v18 src0_sel:BYTE_3
	v_cvt_f32_fp8_e32 v36, v18
	v_cvt_f32_fp8_sdwa v37, v18 src0_sel:BYTE_1
	v_cvt_f32_fp8_e32 v102, v19
	v_cvt_f32_fp8_sdwa v103, v19 src0_sel:BYTE_1
	v_cvt_f32_fp8_sdwa v18, v19 src0_sel:BYTE_2
	v_cvt_f32_fp8_sdwa v19, v19 src0_sel:BYTE_3
	s_waitcnt vmcnt(60)
; #define GAS __attribute__((address_space(1)))
; __device__ __forceinline__ void ln_row(f32x4 (&v)[4], const GAS float* g, const GAS float* b, int lane) {
;     float s = 0.f;
; #pragma unroll
;     for (int j = 0; j < 4; ++j) s += (v[j].x + v[j].y) + (v[j].z + v[j].w);
;     const float mean = wave_sum(s) * (1.f / D); float s2 = 0.f;
; #pragma unroll
;     for (int j = 0; j < 4; ++j) { v[j] = v[j] - mean; s2 += (v[j].x * v[j].x + v[j].y * v[j].y) + (v[j].z * v[j].z + v[j].w * v[j].w); }
;     const float rstd = __builtin_amdgcn_rsqf(wave_sum(s2) * (1.f / D) + LN_EPS);
; #pragma unroll
;     for (int j = 0; j < 4; ++j) { const f32x4 gg = *(const GAS f32x4*)(g + 4 * lane + 256 * j), bb = *(const GAS f32x4*)(b + 4 * lane + 256 * j); v[j] = v[j] * rstd * gg + bb; }
; }
; __device__ __forceinline__ void p7_combine(Frame& F, int l) {
;     ...
;             ln_row(v[r], g2, b2, lane);
;             if (lastl) store_row_f(v[r], F.H + (size_t)(m + r) * D, lane);
;             else store_row_q(v[r], HQ + (size_t)(m + r) * D, HS + m + r, lane); }
	v_cvt_f32_fp8_e32 v104, v20
	v_cvt_f32_fp8_sdwa v105, v20 src0_sel:BYTE_1
	v_cvt_f32_fp8_sdwa v106, v20 src0_sel:BYTE_2
	v_cvt_f32_fp8_sdwa v107, v20 src0_sel:BYTE_3
	v_pk_add_f32 v[20:21], v[22:23], 0 op_sel_hi:[1,0]
	v_pk_add_f32 v[22:23], v[34:35], 0 op_sel_hi:[1,0]
	v_cvt_f32_i32_sdwa v17, sext(v16) dst_sel:DWORD dst_unused:UNUSED_PAD src0_sel:BYTE_3
	v_pk_add_f32 v[22:23], v[22:23], v[100:101]
	v_pk_add_f32 v[20:21], v[20:21], v[36:37]
	v_pk_add_f32 v[18:19], v[22:23], v[18:19]
	v_cvt_f32_i32_sdwa v23, sext(v16) dst_sel:DWORD dst_unused:UNUSED_PAD src0_sel:BYTE_1
	v_cvt_f32_i32_sdwa v22, sext(v16) dst_sel:DWORD dst_unused:UNUSED_PAD src0_sel:BYTE_0
	v_cvt_f32_i32_sdwa v16, sext(v16) dst_sel:DWORD dst_unused:UNUSED_PAD src0_sel:BYTE_2
	v_pk_add_f32 v[20:21], v[20:21], v[102:103]
	v_pk_add_f32 v[18:19], v[18:19], v[106:107]
	v_pk_add_f32 v[20:21], v[20:21], v[104:105]
	v_pk_mul_f32 v[18:19], v[18:19], s[10:11] op_sel_hi:[1,0]
	v_pk_mul_f32 v[20:21], v[20:21], s[10:11] op_sel_hi:[1,0]
	v_pk_fma_f32 v[34:35], v[0:1], v[16:17], v[18:19] op_sel_hi:[0,1,1]
	v_pk_mov_b32 v[16:17], v[6:7], v[4:5] op_sel:[1,0]
	v_mov_b32_e32 v18, v6
	v_mov_b32_e32 v19, v5
	v_pk_fma_f32 v[36:37], v[0:1], v[22:23], v[20:21] op_sel_hi:[0,1,1]
	v_pk_add_f32 v[16:17], v[16:17], v[18:19]
	v_pk_mov_b32 v[18:19], v[10:11], v[8:9] op_sel:[1,0]
	v_mov_b32_e32 v20, v10
	v_mov_b32_e32 v21, v9
	v_pk_add_f32 v[18:19], v[18:19], v[20:21]
	v_add_f32_e32 v0, v16, v17
	v_pk_add_f32 v[18:19], v[18:19], v[18:19] op_sel:[0,1] op_sel_hi:[1,0]
	v_add_f32_e32 v16, 0, v0
	v_add_f32_e32 v20, v14, v15
	v_add_f32_e32 v22, v12, v13
	v_mov_b32_e32 v17, v36
	v_mov_b32_e32 v19, v37
	v_mov_b32_e32 v21, v34
	v_mov_b32_e32 v23, v35
	v_pk_add_f32 v[16:17], v[16:17], v[18:19]
	v_pk_add_f32 v[18:19], v[20:21], v[22:23]
	s_nop 0
	v_pk_add_f32 v[16:17], v[16:17], v[18:19]
	s_nop 0
	v_add_f32_e32 v0, v16, v17
	v_mov_b32_e32 v16, v0
	s_nop 1
	v_mov_b32_dpp v16, v16 quad_perm:[1,0,3,2] row_mask:0xf bank_mask:0xf
	v_add_f32_e32 v0, v0, v16
	v_mov_b32_e32 v16, v0
	s_nop 1
	v_mov_b32_dpp v16, v16 quad_perm:[2,3,0,1] row_mask:0xf bank_mask:0xf
	v_add_f32_e32 v0, v0, v16
	v_mov_b32_e32 v16, v0
	s_nop 1
	v_mov_b32_dpp v16, v16 row_ror:4 row_mask:0xf bank_mask:0xf
	v_add_f32_e32 v0, v0, v16
	v_mov_b32_e32 v16, v0
	s_nop 1
	v_mov_b32_dpp v16, v16 row_ror:8 row_mask:0xf bank_mask:0xf
	v_add_f32_e32 v0, v0, v16
	v_mov_b32_e32 v16, v0
	s_nop 1
	v_mov_b32_dpp v16, v16 row_bcast:15 row_mask:0xa bank_mask:0xf
	v_add_f32_e32 v0, v0, v16
	v_mov_b32_e32 v16, v0
	s_nop 1
	v_mov_b32_dpp v16, v16 row_bcast:31 row_mask:0xc bank_mask:0xf
	v_add_f32_e32 v0, v0, v16
	s_nop 0
	v_readlane_b32 s10, v0, 63
	s_nop 1
	v_fma_f32 v7, s10, v196, v7
	v_fmac_f32_e32 v6, s10, v196
	v_fma_f32 v5, s10, v196, v5
	v_fmac_f32_e32 v4, s10, v196
	v_pk_mul_f32 v[16:17], v[4:5], v[4:5]
	v_pk_mul_f32 v[18:19], v[6:7], v[6:7]
	v_fma_f32 v11, s10, v196, v11
	v_pk_mov_b32 v[20:21], v[18:19], v[16:17] op_sel:[1,0]
	v_mov_b32_e32 v19, v17
	v_fmac_f32_e32 v10, s10, v196
	v_fma_f32 v9, s10, v196, v9
	v_fmac_f32_e32 v8, s10, v196
	v_pk_add_f32 v[16:17], v[20:21], v[18:19]
	v_pk_mul_f32 v[18:19], v[8:9], v[8:9]
	v_pk_mul_f32 v[20:21], v[10:11], v[10:11]
	v_fmac_f32_e32 v14, s10, v196
	v_pk_mov_b32 v[22:23], v[20:21], v[18:19] op_sel:[1,0]
	v_mov_b32_e32 v21, v19
	v_fma_f32 v15, s10, v196, v15
	v_fmac_f32_e32 v12, s10, v196
	v_mul_f32_e32 v0, v14, v14
	v_pk_add_f32 v[18:19], v[22:23], v[20:21]
	v_fma_f32 v13, s10, v196, v13
	v_pk_fma_f32 v[20:21], v[14:15], v[14:15], v[0:1] op_sel_hi:[1,1,0]
	v_mul_f32_e32 v0, v12, v12
	v_pk_add_f32 v[16:17], v[16:17], v[16:17] op_sel_hi:[0,1]
	v_pk_add_f32 v[18:19], v[18:19], v[18:19] op_sel_hi:[0,1]
	v_pk_fma_f32 v[22:23], v[12:13], v[12:13], v[0:1] op_sel_hi:[1,1,0]
	v_fma_f32 v35, s10, v196, v35
	v_fmac_f32_e32 v34, s10, v196
	v_fma_f32 v37, s10, v196, v37
	v_fmac_f32_e32 v36, s10, v196
	v_mul_f32_e32 v20, v36, v36
	v_mul_f32_e32 v22, v37, v37
	v_mul_f32_e32 v16, v34, v34
	v_mul_f32_e32 v18, v35, v35
	v_pk_add_f32 v[20:21], v[20:21], v[22:23]
	v_pk_add_f32 v[16:17], v[16:17], v[18:19]
	s_nop 0
	v_pk_add_f32 v[16:17], v[20:21], v[16:17]
	s_nop 0
	v_add_f32_e32 v0, v16, v17
	v_mov_b32_e32 v16, v0
	s_nop 1
	v_mov_b32_dpp v16, v16 quad_perm:[1,0,3,2] row_mask:0xf bank_mask:0xf
	v_add_f32_e32 v0, v0, v16
	v_mov_b32_e32 v16, v0
	s_nop 1
	v_mov_b32_dpp v16, v16 quad_perm:[2,3,0,1] row_mask:0xf bank_mask:0xf
	v_add_f32_e32 v0, v0, v16
	v_mov_b32_e32 v16, v0
	s_nop 1
	v_mov_b32_dpp v16, v16 row_ror:4 row_mask:0xf bank_mask:0xf
	v_add_f32_e32 v0, v0, v16
	v_mov_b32_e32 v16, v0
	s_nop 1
	v_mov_b32_dpp v16, v16 row_ror:8 row_mask:0xf bank_mask:0xf
	v_add_f32_e32 v0, v0, v16
	v_mov_b32_e32 v16, v0
	s_nop 1
	v_mov_b32_dpp v16, v16 row_bcast:15 row_mask:0xa bank_mask:0xf
	v_add_f32_e32 v0, v0, v16
	v_mov_b32_e32 v16, v0
	s_nop 1
	v_mov_b32_dpp v16, v16 row_bcast:31 row_mask:0xc bank_mask:0xf
	v_add_f32_e32 v0, v0, v16
	s_nop 1
	v_readlane_b32 s10, v0, 63
	s_nop 1
	v_fma_f32 v0, s10, v197, v190
	v_rsq_f32_e32 v0, v0
	s_mov_b64 s[10:11], -1
	v_pk_mul_f32 v[100:101], v[6:7], v[0:1] op_sel_hi:[1,0]
	v_pk_mul_f32 v[4:5], v[4:5], v[0:1] op_sel_hi:[1,0]
	v_pk_mul_f32 v[8:9], v[8:9], v[0:1] op_sel_hi:[1,0]
	v_pk_mul_f32 v[12:13], v[12:13], v[0:1] op_sel_hi:[1,0]
	v_pk_mul_f32 v[36:37], v[36:37], v[0:1] op_sel_hi:[1,0]
	v_pk_mul_f32 v[34:35], v[34:35], v[0:1] op_sel_hi:[1,0]
	s_nop 0
	v_pk_fma_f32 v[6:7], v[206:207], v[4:5], v[222:223]
	v_pk_fma_f32 v[4:5], v[204:205], v[100:101], v[220:221]
	s_nop 1
	v_pk_mul_f32 v[100:101], v[10:11], v[0:1] op_sel_hi:[1,0]
	s_nop 0
	v_pk_fma_f32 v[10:11], v[210:211], v[8:9], v[226:227]
	v_pk_fma_f32 v[8:9], v[208:209], v[100:101], v[224:225]
	s_nop 1
	v_pk_mul_f32 v[100:101], v[14:15], v[0:1] op_sel_hi:[1,0]
	v_cndmask_b32_e64 v0, 0, 1, s[22:23]
	v_cmp_ne_u32_e64 s[36:37], 1, v0
	s_nop 0
	v_pk_fma_f32 v[14:15], v[214:215], v[12:13], v[230:231]
	v_pk_fma_f32 v[12:13], v[212:213], v[100:101], v[228:229]
	s_nop 1
	s_nop 0
	v_pk_fma_f32 v[18:19], v[34:35], v[218:219], v[234:235]
	v_pk_fma_f32 v[16:17], v[36:37], v[216:217], v[232:233]
	v_lshl_add_u64 v[34:35], v[30:31], 0, s[14:15]
	s_cbranch_vccnz .LBB0_1057
	s_mov_b64 s[10:11], 0
	global_store_dwordx4 v[34:35], v[4:7], off
	global_store_dwordx4 v[34:35], v[8:11], off offset:1024
	global_store_dwordx4 v[34:35], v[12:15], off offset:2048
	global_store_dwordx4 v[34:35], v[16:19], off offset:3072

; __device__ __forceinline__ void p7_combine(Frame& F, int l) {
;     ...
;         for (int r = 0; r < 4; ++r) {
; #pragma unroll
;             for (int j = 0; j < 4; ++j) { const int hw = (int)hv[r][j]; f32x4 a; a.x = (float)((hw << 24) >> 24) * hsa[r]; a.y = (float)((hw << 16) >> 24) * hsa[r]; a.z = (float)((hw << 8) >> 24) * hsa[r]; a.w = (float)(hw >> 24) * hsa[r];
;                 f32x4 ys = (f32x4){0.f, 0.f, 0.f, 0.f};
; #pragma unroll
;                 for (int k = 0; k < 4; ++k) { const int w = (int)yv[r][k][j]; ys.x += __builtin_amdgcn_cvt_f32_fp8(w, 0); ys.y += __builtin_amdgcn_cvt_f32_fp8(w, 1); ys.z += __builtin_amdgcn_cvt_f32_fp8(w, 2); ys.w += __builtin_amdgcn_cvt_f32_fp8(w, 3); }
;                 v[r][j] = a + ys * (1.0f / 16.0f); }
.LBB0_1061:
	s_waitcnt vmcnt(40)
	v_mul_f32_e32 v16, 0x3fb504f3, v1
	v_cvt_f32_fp8_e32 v0, v95
	v_cvt_f32_fp8_sdwa v1, v95 src0_sel:BYTE_1
	v_cvt_f32_fp8_sdwa v4, v95 src0_sel:BYTE_2
	v_cvt_f32_fp8_sdwa v5, v95 src0_sel:BYTE_3
	v_cvt_f32_fp8_e32 v6, v96
	v_cvt_f32_fp8_sdwa v7, v96 src0_sel:BYTE_1
	v_cvt_f32_fp8_sdwa v8, v96 src0_sel:BYTE_2
	v_cvt_f32_fp8_sdwa v9, v96 src0_sel:BYTE_3
	v_cvt_f32_fp8_e32 v10, v97
	v_cvt_f32_fp8_sdwa v11, v97 src0_sel:BYTE_1
	v_cvt_f32_fp8_sdwa v12, v97 src0_sel:BYTE_2
	v_cvt_f32_fp8_sdwa v13, v97 src0_sel:BYTE_3
	v_cvt_f32_fp8_e32 v14, v98
	v_cvt_f32_fp8_sdwa v15, v98 src0_sel:BYTE_1
	v_cvt_f32_fp8_sdwa v18, v98 src0_sel:BYTE_2
	v_cvt_f32_fp8_sdwa v19, v98 src0_sel:BYTE_3
	v_pk_add_f32 v[0:1], v[0:1], 0 op_sel_hi:[1,0]
	v_pk_add_f32 v[4:5], v[4:5], 0 op_sel_hi:[1,0]
	v_pk_add_f32 v[0:1], v[0:1], v[6:7]
	v_pk_add_f32 v[4:5], v[4:5], v[8:9]
	v_cvt_f32_i32_sdwa v7, sext(v94) dst_sel:DWORD dst_unused:UNUSED_PAD src0_sel:BYTE_3
	v_cvt_f32_i32_sdwa v9, sext(v94) dst_sel:DWORD dst_unused:UNUSED_PAD src0_sel:BYTE_1
	v_cvt_f32_i32_sdwa v8, sext(v94) dst_sel:DWORD dst_unused:UNUSED_PAD src0_sel:BYTE_0
	v_cvt_f32_i32_sdwa v6, sext(v94) dst_sel:DWORD dst_unused:UNUSED_PAD src0_sel:BYTE_2
	v_pk_add_f32 v[0:1], v[0:1], v[10:11]
	v_pk_add_f32 v[4:5], v[4:5], v[12:13]
	v_pk_add_f32 v[0:1], v[0:1], v[14:15]
	v_pk_add_f32 v[4:5], v[4:5], v[18:19]
	s_mov_b32 s10, 0x3d800000
	v_pk_mul_f32 v[0:1], v[0:1], s[10:11] op_sel_hi:[1,0]
	v_pk_mul_f32 v[4:5], v[4:5], s[10:11] op_sel_hi:[1,0]
	v_cvt_f32_fp8_e32 v10, v91
	v_pk_fma_f32 v[4:5], v[16:17], v[6:7], v[4:5] op_sel_hi:[0,1,1]
	v_pk_fma_f32 v[6:7], v[16:17], v[8:9], v[0:1] op_sel_hi:[0,1,1]
	v_cvt_f32_fp8_e32 v0, v90
	v_cvt_f32_fp8_sdwa v1, v90 src0_sel:BYTE_1
	v_cvt_f32_fp8_sdwa v8, v90 src0_sel:BYTE_2
	v_cvt_f32_fp8_sdwa v9, v90 src0_sel:BYTE_3
	v_cvt_f32_fp8_sdwa v11, v91 src0_sel:BYTE_1
	v_cvt_f32_fp8_sdwa v12, v91 src0_sel:BYTE_2
	v_cvt_f32_fp8_sdwa v13, v91 src0_sel:BYTE_3
	v_cvt_f32_fp8_e32 v14, v92
	v_cvt_f32_fp8_sdwa v15, v92 src0_sel:BYTE_1
	v_cvt_f32_fp8_sdwa v18, v92 src0_sel:BYTE_2
	v_cvt_f32_fp8_sdwa v19, v92 src0_sel:BYTE_3
	v_cvt_f32_fp8_e32 v20, v93
	v_cvt_f32_fp8_sdwa v21, v93 src0_sel:BYTE_1
	v_cvt_f32_fp8_sdwa v22, v93 src0_sel:BYTE_2
	v_cvt_f32_fp8_sdwa v23, v93 src0_sel:BYTE_3
	v_pk_add_f32 v[0:1], v[0:1], 0 op_sel_hi:[1,0]
	v_pk_add_f32 v[8:9], v[8:9], 0 op_sel_hi:[1,0]
	v_pk_add_f32 v[0:1], v[0:1], v[10:11]
	v_pk_add_f32 v[8:9], v[8:9], v[12:13]
	v_cvt_f32_i32_sdwa v11, sext(v89) dst_sel:DWORD dst_unused:UNUSED_PAD src0_sel:BYTE_3
	v_cvt_f32_i32_sdwa v13, sext(v89) dst_sel:DWORD dst_unused:UNUSED_PAD src0_sel:BYTE_1
	v_cvt_f32_i32_sdwa v12, sext(v89) dst_sel:DWORD dst_unused:UNUSED_PAD src0_sel:BYTE_0
	v_cvt_f32_i32_sdwa v10, sext(v89) dst_sel:DWORD dst_unused:UNUSED_PAD src0_sel:BYTE_2
	v_pk_add_f32 v[0:1], v[0:1], v[14:15]
	v_pk_add_f32 v[8:9], v[8:9], v[18:19]
	v_pk_add_f32 v[0:1], v[0:1], v[20:21]
	v_pk_add_f32 v[8:9], v[8:9], v[22:23]
	v_pk_mul_f32 v[0:1], v[0:1], s[10:11] op_sel_hi:[1,0]
	v_pk_mul_f32 v[8:9], v[8:9], s[10:11] op_sel_hi:[1,0]
	v_cvt_f32_fp8_e32 v14, v86
	v_pk_fma_f32 v[8:9], v[16:17], v[10:11], v[8:9] op_sel_hi:[0,1,1]
	v_pk_fma_f32 v[10:11], v[16:17], v[12:13], v[0:1] op_sel_hi:[0,1,1]
	v_cvt_f32_fp8_e32 v0, v85
	v_cvt_f32_fp8_sdwa v1, v85 src0_sel:BYTE_1
	v_cvt_f32_fp8_sdwa v12, v85 src0_sel:BYTE_2
	v_cvt_f32_fp8_sdwa v13, v85 src0_sel:BYTE_3
	v_cvt_f32_fp8_sdwa v15, v86 src0_sel:BYTE_1
	v_cvt_f32_fp8_sdwa v18, v86 src0_sel:BYTE_2
	v_cvt_f32_fp8_sdwa v19, v86 src0_sel:BYTE_3
	v_cvt_f32_fp8_e32 v20, v87
	v_cvt_f32_fp8_sdwa v21, v87 src0_sel:BYTE_1
	v_cvt_f32_fp8_sdwa v22, v87 src0_sel:BYTE_2
	v_cvt_f32_fp8_sdwa v23, v87 src0_sel:BYTE_3
	v_cvt_f32_fp8_e32 v36, v88
	v_cvt_f32_fp8_sdwa v37, v88 src0_sel:BYTE_1
	v_cvt_f32_fp8_sdwa v86, v88 src0_sel:BYTE_2
	v_cvt_f32_fp8_sdwa v87, v88 src0_sel:BYTE_3
	v_pk_add_f32 v[0:1], v[0:1], 0 op_sel_hi:[1,0]
	v_pk_add_f32 v[12:13], v[12:13], 0 op_sel_hi:[1,0]
	v_pk_add_f32 v[0:1], v[0:1], v[14:15]
	v_pk_add_f32 v[12:13], v[12:13], v[18:19]
	v_cvt_f32_i32_sdwa v15, sext(v84) dst_sel:DWORD dst_unused:UNUSED_PAD src0_sel:BYTE_3
	v_cvt_f32_i32_sdwa v19, sext(v84) dst_sel:DWORD dst_unused:UNUSED_PAD src0_sel:BYTE_1
	v_cvt_f32_i32_sdwa v18, sext(v84) dst_sel:DWORD dst_unused:UNUSED_PAD src0_sel:BYTE_0
	v_cvt_f32_i32_sdwa v14, sext(v84) dst_sel:DWORD dst_unused:UNUSED_PAD src0_sel:BYTE_2
	v_pk_add_f32 v[0:1], v[0:1], v[20:21]
	v_pk_add_f32 v[12:13], v[12:13], v[22:23]
	v_pk_add_f32 v[0:1], v[0:1], v[36:37]
	v_pk_add_f32 v[12:13], v[12:13], v[86:87]
	v_pk_mul_f32 v[0:1], v[0:1], s[10:11] op_sel_hi:[1,0]
	v_pk_mul_f32 v[12:13], v[12:13], s[10:11] op_sel_hi:[1,0]
	v_cvt_f32_fp8_e32 v20, v81
	v_pk_fma_f32 v[12:13], v[16:17], v[14:15], v[12:13] op_sel_hi:[0,1,1]
	v_pk_fma_f32 v[14:15], v[16:17], v[18:19], v[0:1] op_sel_hi:[0,1,1]
	v_cvt_f32_fp8_e32 v0, v80
	v_cvt_f32_fp8_sdwa v1, v80 src0_sel:BYTE_1
	v_cvt_f32_fp8_sdwa v18, v80 src0_sel:BYTE_2
	v_cvt_f32_fp8_sdwa v19, v80 src0_sel:BYTE_3
	v_cvt_f32_fp8_sdwa v21, v81 src0_sel:BYTE_1
	v_cvt_f32_fp8_sdwa v22, v81 src0_sel:BYTE_2
	v_cvt_f32_fp8_sdwa v23, v81 src0_sel:BYTE_3
	v_cvt_f32_fp8_e32 v36, v82
	v_cvt_f32_fp8_sdwa v37, v82 src0_sel:BYTE_1
	v_cvt_f32_fp8_sdwa v80, v82 src0_sel:BYTE_2
	v_cvt_f32_fp8_sdwa v81, v82 src0_sel:BYTE_3
	v_cvt_f32_fp8_e32 v84, v83
	v_cvt_f32_fp8_sdwa v85, v83 src0_sel:BYTE_1
	v_cvt_f32_fp8_sdwa v82, v83 src0_sel:BYTE_2
	v_cvt_f32_fp8_sdwa v83, v83 src0_sel:BYTE_3
	v_pk_add_f32 v[0:1], v[0:1], 0 op_sel_hi:[1,0]
	v_pk_add_f32 v[18:19], v[18:19], 0 op_sel_hi:[1,0]
	v_pk_add_f32 v[0:1], v[0:1], v[20:21]
	v_pk_add_f32 v[18:19], v[18:19], v[22:23]
; #define GAS __attribute__((address_space(1)))
; __device__ __forceinline__ void ln_row(f32x4 (&v)[4], const GAS float* g, const GAS float* b, int lane) {
;     float s = 0.f;
; #pragma unroll
;     for (int j = 0; j < 4; ++j) s += (v[j].x + v[j].y) + (v[j].z + v[j].w);
;     const float mean = wave_sum(s) * (1.f / D); float s2 = 0.f;
; #pragma unroll
;     for (int j = 0; j < 4; ++j) { v[j] = v[j] - mean; s2 += (v[j].x * v[j].x + v[j].y * v[j].y) + (v[j].z * v[j].z + v[j].w * v[j].w); }
;     const float rstd = __builtin_amdgcn_rsqf(wave_sum(s2) * (1.f / D) + LN_EPS);
; #pragma unroll
;     for (int j = 0; j < 4; ++j) { const f32x4 gg = *(const GAS f32x4*)(g + 4 * lane + 256 * j), bb = *(const GAS f32x4*)(b + 4 * lane + 256 * j); v[j] = v[j] * rstd * gg + bb; }
; }
; __device__ __forceinline__ void p7_combine(Frame& F, int l) {
;     ...
;             ln_row(v[r], g2, b2, lane);
;             if (lastl) store_row_f(v[r], F.H + (size_t)(m + r) * D, lane);
;             else store_row_q(v[r], HQ + (size_t)(m + r) * D, HS + m + r, lane); }
	v_cvt_f32_i32_sdwa v21, sext(v38) dst_sel:DWORD dst_unused:UNUSED_PAD src0_sel:BYTE_3
	v_cvt_f32_i32_sdwa v23, sext(v38) dst_sel:DWORD dst_unused:UNUSED_PAD src0_sel:BYTE_1
	v_cvt_f32_i32_sdwa v22, sext(v38) dst_sel:DWORD dst_unused:UNUSED_PAD src0_sel:BYTE_0
	v_cvt_f32_i32_sdwa v20, sext(v38) dst_sel:DWORD dst_unused:UNUSED_PAD src0_sel:BYTE_2
	v_pk_add_f32 v[0:1], v[0:1], v[36:37]
	v_pk_add_f32 v[18:19], v[18:19], v[80:81]
	v_pk_add_f32 v[0:1], v[0:1], v[84:85]
	v_pk_add_f32 v[18:19], v[18:19], v[82:83]
	v_pk_mul_f32 v[36:37], v[0:1], s[10:11] op_sel_hi:[1,0]
	v_pk_mul_f32 v[0:1], v[18:19], s[10:11] op_sel_hi:[1,0]
	v_pk_fma_f32 v[36:37], v[16:17], v[22:23], v[36:37] op_sel_hi:[0,1,1]
	v_pk_fma_f32 v[0:1], v[16:17], v[20:21], v[0:1] op_sel_hi:[0,1,1]
	v_pk_mov_b32 v[16:17], v[6:7], v[4:5] op_sel:[1,0]
	v_mov_b32_e32 v18, v6
	v_mov_b32_e32 v19, v5
	v_pk_add_f32 v[16:17], v[16:17], v[18:19]
	v_pk_mov_b32 v[18:19], v[10:11], v[8:9] op_sel:[1,0]
	v_mov_b32_e32 v20, v10
	v_mov_b32_e32 v21, v9
	v_pk_add_f32 v[18:19], v[18:19], v[20:21]
	v_add_f32_e32 v16, v16, v17
	v_pk_add_f32 v[18:19], v[18:19], v[18:19] op_sel:[0,1] op_sel_hi:[1,0]
	v_add_f32_e32 v16, 0, v16
	v_add_f32_e32 v20, v14, v15
	v_add_f32_e32 v22, v12, v13
	v_mov_b32_e32 v17, v36
	v_mov_b32_e32 v19, v37
	v_mov_b32_e32 v21, v0
	v_mov_b32_e32 v23, v1
	v_pk_add_f32 v[16:17], v[16:17], v[18:19]
	v_pk_add_f32 v[18:19], v[20:21], v[22:23]
	s_and_b64 vcc, exec, s[36:37]
	v_pk_add_f32 v[16:17], v[16:17], v[18:19]
	s_nop 0
	v_add_f32_e32 v16, v16, v17
	v_mov_b32_e32 v17, v16
	s_nop 1
	v_mov_b32_dpp v17, v17 quad_perm:[1,0,3,2] row_mask:0xf bank_mask:0xf
	v_add_f32_e32 v16, v16, v17
	v_mov_b32_e32 v17, v16
	s_nop 1
	v_mov_b32_dpp v17, v17 quad_perm:[2,3,0,1] row_mask:0xf bank_mask:0xf
	v_add_f32_e32 v16, v16, v17
	v_mov_b32_e32 v17, v16
	s_nop 1
	v_mov_b32_dpp v17, v17 row_ror:4 row_mask:0xf bank_mask:0xf
	v_add_f32_e32 v16, v16, v17
	v_mov_b32_e32 v17, v16
	s_nop 1
	v_mov_b32_dpp v17, v17 row_ror:8 row_mask:0xf bank_mask:0xf
	v_add_f32_e32 v16, v16, v17
	v_mov_b32_e32 v17, v16
	s_nop 1
	v_mov_b32_dpp v17, v17 row_bcast:15 row_mask:0xa bank_mask:0xf
	v_add_f32_e32 v16, v16, v17
	v_mov_b32_e32 v17, v16
	s_nop 1
	v_mov_b32_dpp v17, v17 row_bcast:31 row_mask:0xc bank_mask:0xf
	v_add_f32_e32 v16, v16, v17
	s_nop 0
	v_readlane_b32 s10, v16, 63
	s_nop 1
	v_fma_f32 v7, s10, v196, v7
	v_fmac_f32_e32 v6, s10, v196
	v_fma_f32 v5, s10, v196, v5
	v_fmac_f32_e32 v4, s10, v196
	v_pk_mul_f32 v[16:17], v[4:5], v[4:5]
	v_pk_mul_f32 v[18:19], v[6:7], v[6:7]
	v_fma_f32 v11, s10, v196, v11
	v_pk_mov_b32 v[20:21], v[18:19], v[16:17] op_sel:[1,0]
	v_mov_b32_e32 v19, v17
	v_pk_add_f32 v[16:17], v[20:21], v[18:19]
	v_fmac_f32_e32 v10, s10, v196
	v_fma_f32 v9, s10, v196, v9
	v_fmac_f32_e32 v8, s10, v196
	v_pk_add_f32 v[16:17], v[16:17], v[16:17] op_sel_hi:[0,1]
	v_pk_mul_f32 v[18:19], v[8:9], v[8:9]
	v_pk_mul_f32 v[20:21], v[10:11], v[10:11]
	v_fmac_f32_e32 v14, s10, v196
	v_pk_mov_b32 v[22:23], v[20:21], v[18:19] op_sel:[1,0]
	v_mov_b32_e32 v21, v19
	v_fma_f32 v15, s10, v196, v15
	v_fmac_f32_e32 v12, s10, v196
	v_mul_f32_e32 v16, v14, v14
	v_pk_add_f32 v[18:19], v[22:23], v[20:21]
	v_fma_f32 v13, s10, v196, v13
	v_pk_fma_f32 v[20:21], v[14:15], v[14:15], v[16:17] op_sel_hi:[1,1,0]
	v_mul_f32_e32 v16, v12, v12
	v_pk_add_f32 v[18:19], v[18:19], v[18:19] op_sel_hi:[0,1]
	v_pk_fma_f32 v[22:23], v[12:13], v[12:13], v[16:17] op_sel_hi:[1,1,0]
	v_fma_f32 v1, s10, v196, v1
	v_fmac_f32_e32 v0, s10, v196
	v_fma_f32 v37, s10, v196, v37
	v_fmac_f32_e32 v36, s10, v196
	v_mul_f32_e32 v20, v36, v36
	v_mul_f32_e32 v22, v37, v37
	v_mul_f32_e32 v16, v0, v0
	v_mul_f32_e32 v18, v1, v1
	v_pk_add_f32 v[20:21], v[20:21], v[22:23]
	v_pk_add_f32 v[16:17], v[16:17], v[18:19]
	s_nop 0
	v_pk_add_f32 v[16:17], v[20:21], v[16:17]
	s_nop 0
	v_add_f32_e32 v16, v16, v17
	v_mov_b32_e32 v17, v16
	s_nop 1
	v_mov_b32_dpp v17, v17 quad_perm:[1,0,3,2] row_mask:0xf bank_mask:0xf
	v_add_f32_e32 v16, v16, v17
	v_mov_b32_e32 v17, v16
	s_nop 1
	v_mov_b32_dpp v17, v17 quad_perm:[2,3,0,1] row_mask:0xf bank_mask:0xf
	v_add_f32_e32 v16, v16, v17
	v_mov_b32_e32 v17, v16
	s_nop 1
	v_mov_b32_dpp v17, v17 row_ror:4 row_mask:0xf bank_mask:0xf
	v_add_f32_e32 v16, v16, v17
	v_mov_b32_e32 v17, v16
	s_nop 1
	v_mov_b32_dpp v17, v17 row_ror:8 row_mask:0xf bank_mask:0xf
	v_add_f32_e32 v16, v16, v17
	v_mov_b32_e32 v17, v16
	s_nop 1
	v_mov_b32_dpp v17, v17 row_bcast:15 row_mask:0xa bank_mask:0xf
	v_add_f32_e32 v16, v16, v17
	v_mov_b32_e32 v17, v16
	s_nop 1
	v_mov_b32_dpp v17, v17 row_bcast:31 row_mask:0xc bank_mask:0xf
	v_add_f32_e32 v16, v16, v17
	s_nop 0
	v_readlane_b32 s10, v16, 63
	s_nop 1
	v_fma_f32 v16, s10, v197, v190
	v_rsq_f32_e32 v38, v16
	s_nop 1
	s_mov_b64 s[10:11], -1
	v_pk_mul_f32 v[80:81], v[6:7], v[38:39] op_sel_hi:[1,0]
	v_pk_mul_f32 v[4:5], v[4:5], v[38:39] op_sel_hi:[1,0]
	v_pk_mul_f32 v[8:9], v[8:9], v[38:39] op_sel_hi:[1,0]
	v_pk_mul_f32 v[12:13], v[12:13], v[38:39] op_sel_hi:[1,0]
	v_pk_mul_f32 v[36:37], v[36:37], v[38:39] op_sel_hi:[1,0]
	v_pk_mul_f32 v[0:1], v[0:1], v[38:39] op_sel_hi:[1,0]
	s_nop 0
	v_pk_fma_f32 v[6:7], v[206:207], v[4:5], v[222:223]
	v_pk_fma_f32 v[4:5], v[204:205], v[80:81], v[220:221]
	s_nop 1
	v_pk_mul_f32 v[80:81], v[10:11], v[38:39] op_sel_hi:[1,0]
	s_nop 0
	v_pk_fma_f32 v[10:11], v[210:211], v[8:9], v[226:227]
	v_pk_fma_f32 v[8:9], v[208:209], v[80:81], v[224:225]
	s_nop 1
	v_pk_mul_f32 v[80:81], v[14:15], v[38:39] op_sel_hi:[1,0]
	s_nop 0
	v_pk_fma_f32 v[14:15], v[214:215], v[12:13], v[230:231]
	v_pk_fma_f32 v[12:13], v[212:213], v[80:81], v[228:229]
	s_nop 1
	s_nop 0
	v_pk_fma_f32 v[18:19], v[0:1], v[218:219], v[234:235]
	v_pk_fma_f32 v[16:17], v[36:37], v[216:217], v[232:233]
	s_cbranch_vccnz .LBB0_1063
	v_add_co_u32_e32 v0, vcc, 0x1000, v34
	s_mov_b64 s[10:11], 0
	s_nop 0
	v_addc_co_u32_e32 v1, vcc, 0, v35, vcc
	global_store_dwordx4 v[0:1], v[4:7], off
	global_store_dwordx4 v[0:1], v[8:11], off offset:1024
	global_store_dwordx4 v[0:1], v[12:15], off offset:2048
	global_store_dwordx4 v[0:1], v[16:19], off offset:3072

; __device__ __forceinline__ void p7_combine(Frame& F, int l) {
;     ...
;         for (int r = 0; r < 4; ++r) {
; #pragma unroll
;             for (int j = 0; j < 4; ++j) { const int hw = (int)hv[r][j]; f32x4 a; a.x = (float)((hw << 24) >> 24) * hsa[r]; a.y = (float)((hw << 16) >> 24) * hsa[r]; a.z = (float)((hw << 8) >> 24) * hsa[r]; a.w = (float)(hw >> 24) * hsa[r];
;                 f32x4 ys = (f32x4){0.f, 0.f, 0.f, 0.f};
; #pragma unroll
;                 for (int k = 0; k < 4; ++k) { const int w = (int)yv[r][k][j]; ys.x += __builtin_amdgcn_cvt_f32_fp8(w, 0); ys.y += __builtin_amdgcn_cvt_f32_fp8(w, 1); ys.z += __builtin_amdgcn_cvt_f32_fp8(w, 2); ys.w += __builtin_amdgcn_cvt_f32_fp8(w, 3); }
;                 v[r][j] = a + ys * (1.0f / 16.0f); }
.LBB0_1067:
	s_waitcnt vmcnt(20)
	v_cvt_f32_fp8_e32 v0, v76
	v_cvt_f32_fp8_sdwa v1, v76 src0_sel:BYTE_1
	v_cvt_f32_fp8_sdwa v4, v76 src0_sel:BYTE_2
	v_cvt_f32_fp8_sdwa v5, v76 src0_sel:BYTE_3
	v_cvt_f32_fp8_e32 v6, v77
	v_cvt_f32_fp8_sdwa v7, v77 src0_sel:BYTE_1
	v_cvt_f32_fp8_sdwa v8, v77 src0_sel:BYTE_2
	v_cvt_f32_fp8_sdwa v9, v77 src0_sel:BYTE_3
	v_cvt_f32_fp8_e32 v10, v78
	v_cvt_f32_fp8_sdwa v11, v78 src0_sel:BYTE_1
	v_cvt_f32_fp8_sdwa v12, v78 src0_sel:BYTE_2
	v_cvt_f32_fp8_sdwa v13, v78 src0_sel:BYTE_3
	v_cvt_f32_fp8_e32 v14, v79
	v_cvt_f32_fp8_sdwa v15, v79 src0_sel:BYTE_1
	v_cvt_f32_fp8_sdwa v16, v79 src0_sel:BYTE_2
	v_cvt_f32_fp8_sdwa v17, v79 src0_sel:BYTE_3
	v_pk_add_f32 v[0:1], v[0:1], 0 op_sel_hi:[1,0]
	v_pk_add_f32 v[4:5], v[4:5], 0 op_sel_hi:[1,0]
	v_pk_add_f32 v[0:1], v[0:1], v[6:7]
	v_pk_add_f32 v[4:5], v[4:5], v[8:9]
	v_cvt_f32_i32_sdwa v7, sext(v75) dst_sel:DWORD dst_unused:UNUSED_PAD src0_sel:BYTE_3
	v_cvt_f32_i32_sdwa v9, sext(v75) dst_sel:DWORD dst_unused:UNUSED_PAD src0_sel:BYTE_1
	v_cvt_f32_i32_sdwa v8, sext(v75) dst_sel:DWORD dst_unused:UNUSED_PAD src0_sel:BYTE_0
	v_cvt_f32_i32_sdwa v6, sext(v75) dst_sel:DWORD dst_unused:UNUSED_PAD src0_sel:BYTE_2
	v_pk_add_f32 v[0:1], v[0:1], v[10:11]
	v_pk_add_f32 v[4:5], v[4:5], v[12:13]
	v_pk_add_f32 v[0:1], v[0:1], v[14:15]
	v_pk_add_f32 v[4:5], v[4:5], v[16:17]
	s_mov_b32 s10, 0x3d800000
	v_mul_f32_e32 v2, 0x3fb504f3, v2
	v_pk_mul_f32 v[0:1], v[0:1], s[10:11] op_sel_hi:[1,0]
	v_pk_mul_f32 v[4:5], v[4:5], s[10:11] op_sel_hi:[1,0]
	v_cvt_f32_fp8_e32 v10, v72
	v_pk_fma_f32 v[4:5], v[2:3], v[6:7], v[4:5] op_sel_hi:[0,1,1]
	v_pk_fma_f32 v[6:7], v[2:3], v[8:9], v[0:1] op_sel_hi:[0,1,1]
	v_cvt_f32_fp8_e32 v0, v71
	v_cvt_f32_fp8_sdwa v1, v71 src0_sel:BYTE_1
	v_cvt_f32_fp8_sdwa v8, v71 src0_sel:BYTE_2
	v_cvt_f32_fp8_sdwa v9, v71 src0_sel:BYTE_3
	v_cvt_f32_fp8_sdwa v11, v72 src0_sel:BYTE_1
	v_cvt_f32_fp8_sdwa v12, v72 src0_sel:BYTE_2
	v_cvt_f32_fp8_sdwa v13, v72 src0_sel:BYTE_3
	v_cvt_f32_fp8_e32 v14, v73
	v_cvt_f32_fp8_sdwa v15, v73 src0_sel:BYTE_1
	v_cvt_f32_fp8_sdwa v16, v73 src0_sel:BYTE_2
	v_cvt_f32_fp8_sdwa v17, v73 src0_sel:BYTE_3
	v_cvt_f32_fp8_e32 v18, v74
	v_cvt_f32_fp8_sdwa v19, v74 src0_sel:BYTE_1
	v_cvt_f32_fp8_sdwa v20, v74 src0_sel:BYTE_2
	v_cvt_f32_fp8_sdwa v21, v74 src0_sel:BYTE_3
	v_pk_add_f32 v[0:1], v[0:1], 0 op_sel_hi:[1,0]
	v_pk_add_f32 v[8:9], v[8:9], 0 op_sel_hi:[1,0]
	v_pk_add_f32 v[0:1], v[0:1], v[10:11]
	v_pk_add_f32 v[8:9], v[8:9], v[12:13]
	v_cvt_f32_i32_sdwa v11, sext(v70) dst_sel:DWORD dst_unused:UNUSED_PAD src0_sel:BYTE_3
	v_cvt_f32_i32_sdwa v13, sext(v70) dst_sel:DWORD dst_unused:UNUSED_PAD src0_sel:BYTE_1
	v_cvt_f32_i32_sdwa v12, sext(v70) dst_sel:DWORD dst_unused:UNUSED_PAD src0_sel:BYTE_0
	v_cvt_f32_i32_sdwa v10, sext(v70) dst_sel:DWORD dst_unused:UNUSED_PAD src0_sel:BYTE_2
	v_pk_add_f32 v[0:1], v[0:1], v[14:15]
	v_pk_add_f32 v[8:9], v[8:9], v[16:17]
	v_pk_add_f32 v[0:1], v[0:1], v[18:19]
	v_pk_add_f32 v[8:9], v[8:9], v[20:21]
	v_pk_mul_f32 v[0:1], v[0:1], s[10:11] op_sel_hi:[1,0]
	v_pk_mul_f32 v[8:9], v[8:9], s[10:11] op_sel_hi:[1,0]
	v_cvt_f32_fp8_e32 v14, v67
	v_pk_fma_f32 v[8:9], v[2:3], v[10:11], v[8:9] op_sel_hi:[0,1,1]
	v_pk_fma_f32 v[10:11], v[2:3], v[12:13], v[0:1] op_sel_hi:[0,1,1]
	v_cvt_f32_fp8_e32 v0, v66
	v_cvt_f32_fp8_sdwa v1, v66 src0_sel:BYTE_1
	v_cvt_f32_fp8_sdwa v12, v66 src0_sel:BYTE_2
	v_cvt_f32_fp8_sdwa v13, v66 src0_sel:BYTE_3
	v_cvt_f32_fp8_sdwa v15, v67 src0_sel:BYTE_1
	v_cvt_f32_fp8_sdwa v16, v67 src0_sel:BYTE_2
	v_cvt_f32_fp8_sdwa v17, v67 src0_sel:BYTE_3
	v_cvt_f32_fp8_e32 v18, v68
	v_cvt_f32_fp8_sdwa v19, v68 src0_sel:BYTE_1
	v_cvt_f32_fp8_sdwa v20, v68 src0_sel:BYTE_2
	v_cvt_f32_fp8_sdwa v21, v68 src0_sel:BYTE_3
	v_cvt_f32_fp8_e32 v22, v69
	v_cvt_f32_fp8_sdwa v23, v69 src0_sel:BYTE_1
	v_cvt_f32_fp8_sdwa v36, v69 src0_sel:BYTE_2
	v_cvt_f32_fp8_sdwa v37, v69 src0_sel:BYTE_3
	v_pk_add_f32 v[0:1], v[0:1], 0 op_sel_hi:[1,0]
	v_pk_add_f32 v[12:13], v[12:13], 0 op_sel_hi:[1,0]
	v_pk_add_f32 v[0:1], v[0:1], v[14:15]
	v_pk_add_f32 v[12:13], v[12:13], v[16:17]
	v_cvt_f32_i32_sdwa v15, sext(v65) dst_sel:DWORD dst_unused:UNUSED_PAD src0_sel:BYTE_3
	v_cvt_f32_i32_sdwa v17, sext(v65) dst_sel:DWORD dst_unused:UNUSED_PAD src0_sel:BYTE_1
	v_cvt_f32_i32_sdwa v16, sext(v65) dst_sel:DWORD dst_unused:UNUSED_PAD src0_sel:BYTE_0
	v_cvt_f32_i32_sdwa v14, sext(v65) dst_sel:DWORD dst_unused:UNUSED_PAD src0_sel:BYTE_2
	v_pk_add_f32 v[0:1], v[0:1], v[18:19]
	v_pk_add_f32 v[12:13], v[12:13], v[20:21]
	v_pk_add_f32 v[0:1], v[0:1], v[22:23]
	v_pk_add_f32 v[12:13], v[12:13], v[36:37]
	v_pk_mul_f32 v[0:1], v[0:1], s[10:11] op_sel_hi:[1,0]
	v_pk_mul_f32 v[12:13], v[12:13], s[10:11] op_sel_hi:[1,0]
	v_cvt_f32_fp8_e32 v18, v62
	v_pk_fma_f32 v[12:13], v[2:3], v[14:15], v[12:13] op_sel_hi:[0,1,1]
	v_pk_fma_f32 v[14:15], v[2:3], v[16:17], v[0:1] op_sel_hi:[0,1,1]
	v_cvt_f32_fp8_e32 v0, v61
	v_cvt_f32_fp8_sdwa v1, v61 src0_sel:BYTE_1
	v_cvt_f32_fp8_sdwa v16, v61 src0_sel:BYTE_2
	v_cvt_f32_fp8_sdwa v17, v61 src0_sel:BYTE_3
	v_cvt_f32_fp8_sdwa v19, v62 src0_sel:BYTE_1
	v_cvt_f32_fp8_sdwa v20, v62 src0_sel:BYTE_2
	v_cvt_f32_fp8_sdwa v21, v62 src0_sel:BYTE_3
	v_cvt_f32_fp8_e32 v22, v63
	v_cvt_f32_fp8_sdwa v23, v63 src0_sel:BYTE_1
	v_cvt_f32_fp8_sdwa v36, v63 src0_sel:BYTE_2
	v_cvt_f32_fp8_sdwa v37, v63 src0_sel:BYTE_3
	v_cvt_f32_fp8_e32 v62, v64
	v_cvt_f32_fp8_sdwa v63, v64 src0_sel:BYTE_1
	v_cvt_f32_fp8_sdwa v66, v64 src0_sel:BYTE_2
	v_cvt_f32_fp8_sdwa v67, v64 src0_sel:BYTE_3
	v_pk_add_f32 v[0:1], v[0:1], 0 op_sel_hi:[1,0]
	v_pk_add_f32 v[16:17], v[16:17], 0 op_sel_hi:[1,0]
	v_pk_add_f32 v[0:1], v[0:1], v[18:19]
	v_pk_add_f32 v[16:17], v[16:17], v[20:21]
; #define GAS __attribute__((address_space(1)))
; __device__ __forceinline__ void ln_row(f32x4 (&v)[4], const GAS float* g, const GAS float* b, int lane) {
;     float s = 0.f;
; #pragma unroll
;     for (int j = 0; j < 4; ++j) s += (v[j].x + v[j].y) + (v[j].z + v[j].w);
;     const float mean = wave_sum(s) * (1.f / D); float s2 = 0.f;
; #pragma unroll
;     for (int j = 0; j < 4; ++j) { v[j] = v[j] - mean; s2 += (v[j].x * v[j].x + v[j].y * v[j].y) + (v[j].z * v[j].z + v[j].w * v[j].w); }
;     const float rstd = __builtin_amdgcn_rsqf(wave_sum(s2) * (1.f / D) + LN_EPS);
; #pragma unroll
;     for (int j = 0; j < 4; ++j) { const f32x4 gg = *(const GAS f32x4*)(g + 4 * lane + 256 * j), bb = *(const GAS f32x4*)(b + 4 * lane + 256 * j); v[j] = v[j] * rstd * gg + bb; }
; }
; __device__ __forceinline__ void p7_combine(Frame& F, int l) {
;     ...
;             ln_row(v[r], g2, b2, lane);
;             if (lastl) store_row_f(v[r], F.H + (size_t)(m + r) * D, lane);
;             else store_row_q(v[r], HQ + (size_t)(m + r) * D, HS + m + r, lane); }
	v_cvt_f32_i32_sdwa v19, sext(v60) dst_sel:DWORD dst_unused:UNUSED_PAD src0_sel:BYTE_3
	v_cvt_f32_i32_sdwa v18, sext(v60) dst_sel:DWORD dst_unused:UNUSED_PAD src0_sel:BYTE_2
	v_pk_add_f32 v[0:1], v[0:1], v[22:23]
	v_pk_add_f32 v[16:17], v[16:17], v[36:37]
	v_cvt_f32_i32_sdwa v21, sext(v60) dst_sel:DWORD dst_unused:UNUSED_PAD src0_sel:BYTE_1
	v_cvt_f32_i32_sdwa v20, sext(v60) dst_sel:DWORD dst_unused:UNUSED_PAD src0_sel:BYTE_0
	v_pk_add_f32 v[16:17], v[16:17], v[66:67]
	v_pk_add_f32 v[0:1], v[0:1], v[62:63]
	s_and_b64 vcc, exec, s[36:37]
	v_pk_mul_f32 v[22:23], v[0:1], s[10:11] op_sel_hi:[1,0]
	v_pk_mul_f32 v[0:1], v[16:17], s[10:11] op_sel_hi:[1,0]
	v_pk_mov_b32 v[16:17], v[6:7], v[4:5] op_sel:[1,0]
	v_pk_fma_f32 v[0:1], v[2:3], v[18:19], v[0:1] op_sel_hi:[0,1,1]
	v_mov_b32_e32 v18, v6
	v_mov_b32_e32 v19, v5
	v_pk_fma_f32 v[36:37], v[2:3], v[20:21], v[22:23] op_sel_hi:[0,1,1]
	v_pk_add_f32 v[16:17], v[16:17], v[18:19]
	v_pk_mov_b32 v[18:19], v[10:11], v[8:9] op_sel:[1,0]
	v_mov_b32_e32 v20, v10
	v_mov_b32_e32 v21, v9
	v_pk_add_f32 v[18:19], v[18:19], v[20:21]
	v_add_f32_e32 v2, v16, v17
	v_pk_add_f32 v[18:19], v[18:19], v[18:19] op_sel:[0,1] op_sel_hi:[1,0]
	v_add_f32_e32 v16, 0, v2
	v_add_f32_e32 v20, v14, v15
	v_add_f32_e32 v22, v12, v13
	v_mov_b32_e32 v17, v36
	v_mov_b32_e32 v19, v37
	v_mov_b32_e32 v21, v0
	v_mov_b32_e32 v23, v1
	v_pk_add_f32 v[16:17], v[16:17], v[18:19]
	v_pk_add_f32 v[18:19], v[20:21], v[22:23]
	s_nop 0
	v_pk_add_f32 v[16:17], v[16:17], v[18:19]
	s_nop 0
	v_add_f32_e32 v2, v16, v17
	v_mov_b32_e32 v16, v2
	s_nop 1
	v_mov_b32_dpp v16, v16 quad_perm:[1,0,3,2] row_mask:0xf bank_mask:0xf
	v_add_f32_e32 v2, v2, v16
	v_mov_b32_e32 v16, v2
	s_nop 1
	v_mov_b32_dpp v16, v16 quad_perm:[2,3,0,1] row_mask:0xf bank_mask:0xf
	v_add_f32_e32 v2, v2, v16
	v_mov_b32_e32 v16, v2
	s_nop 1
	v_mov_b32_dpp v16, v16 row_ror:4 row_mask:0xf bank_mask:0xf
	v_add_f32_e32 v2, v2, v16
	v_mov_b32_e32 v16, v2
	s_nop 1
	v_mov_b32_dpp v16, v16 row_ror:8 row_mask:0xf bank_mask:0xf
	v_add_f32_e32 v2, v2, v16
	v_mov_b32_e32 v16, v2
	s_nop 1
	v_mov_b32_dpp v16, v16 row_bcast:15 row_mask:0xa bank_mask:0xf
	v_add_f32_e32 v2, v2, v16
	v_mov_b32_e32 v16, v2
	s_nop 1
	v_mov_b32_dpp v16, v16 row_bcast:31 row_mask:0xc bank_mask:0xf
	v_add_f32_e32 v2, v2, v16
	s_nop 0
	v_readlane_b32 s10, v2, 63
	s_nop 1
	v_fma_f32 v7, s10, v196, v7
	v_fmac_f32_e32 v6, s10, v196
	v_fma_f32 v5, s10, v196, v5
	v_fmac_f32_e32 v4, s10, v196
	v_pk_mul_f32 v[16:17], v[4:5], v[4:5]
	v_pk_mul_f32 v[18:19], v[6:7], v[6:7]
	v_fma_f32 v11, s10, v196, v11
	v_pk_mov_b32 v[20:21], v[18:19], v[16:17] op_sel:[1,0]
	v_mov_b32_e32 v19, v17
	v_fmac_f32_e32 v10, s10, v196
	v_fma_f32 v9, s10, v196, v9
	v_fmac_f32_e32 v8, s10, v196
	v_pk_add_f32 v[16:17], v[20:21], v[18:19]
	v_pk_mul_f32 v[18:19], v[8:9], v[8:9]
	v_pk_mul_f32 v[20:21], v[10:11], v[10:11]
	v_fmac_f32_e32 v14, s10, v196
	v_pk_mov_b32 v[22:23], v[20:21], v[18:19] op_sel:[1,0]
	v_mov_b32_e32 v21, v19
	v_fma_f32 v15, s10, v196, v15
	v_fmac_f32_e32 v12, s10, v196
	v_mul_f32_e32 v2, v14, v14
	v_pk_add_f32 v[18:19], v[22:23], v[20:21]
	v_fma_f32 v13, s10, v196, v13
	v_pk_fma_f32 v[20:21], v[14:15], v[14:15], v[2:3] op_sel_hi:[1,1,0]
	v_mul_f32_e32 v2, v12, v12
	v_pk_add_f32 v[16:17], v[16:17], v[16:17] op_sel_hi:[0,1]
	v_pk_add_f32 v[18:19], v[18:19], v[18:19] op_sel_hi:[0,1]
	v_pk_fma_f32 v[22:23], v[12:13], v[12:13], v[2:3] op_sel_hi:[1,1,0]
	v_fma_f32 v1, s10, v196, v1
	v_fmac_f32_e32 v0, s10, v196
	v_fma_f32 v37, s10, v196, v37
	v_fmac_f32_e32 v36, s10, v196
	v_mul_f32_e32 v20, v36, v36
	v_mul_f32_e32 v22, v37, v37
	v_mul_f32_e32 v16, v0, v0
	v_mul_f32_e32 v18, v1, v1
	v_pk_add_f32 v[20:21], v[20:21], v[22:23]
	v_pk_add_f32 v[16:17], v[16:17], v[18:19]
	s_nop 0
	v_pk_add_f32 v[16:17], v[20:21], v[16:17]
	s_nop 0
	v_add_f32_e32 v2, v16, v17
	v_mov_b32_e32 v16, v2
	s_nop 1
	v_mov_b32_dpp v16, v16 quad_perm:[1,0,3,2] row_mask:0xf bank_mask:0xf
	v_add_f32_e32 v2, v2, v16
	v_mov_b32_e32 v16, v2
	s_nop 1
	v_mov_b32_dpp v16, v16 quad_perm:[2,3,0,1] row_mask:0xf bank_mask:0xf
	v_add_f32_e32 v2, v2, v16
	v_mov_b32_e32 v16, v2
	s_nop 1
	v_mov_b32_dpp v16, v16 row_ror:4 row_mask:0xf bank_mask:0xf
	v_add_f32_e32 v2, v2, v16
	v_mov_b32_e32 v16, v2
	s_nop 1
	v_mov_b32_dpp v16, v16 row_ror:8 row_mask:0xf bank_mask:0xf
	v_add_f32_e32 v2, v2, v16
	v_mov_b32_e32 v16, v2
	s_nop 1
	v_mov_b32_dpp v16, v16 row_bcast:15 row_mask:0xa bank_mask:0xf
	v_add_f32_e32 v2, v2, v16
	v_mov_b32_e32 v16, v2
	s_nop 1
	v_mov_b32_dpp v16, v16 row_bcast:31 row_mask:0xc bank_mask:0xf
	v_add_f32_e32 v2, v2, v16
	s_nop 1
	v_readlane_b32 s10, v2, 63
	s_nop 1
	v_fma_f32 v2, s10, v197, v190
	v_rsq_f32_e32 v2, v2
	s_mov_b64 s[10:11], -1
	v_pk_mul_f32 v[60:61], v[6:7], v[2:3] op_sel_hi:[1,0]
	v_pk_mul_f32 v[4:5], v[4:5], v[2:3] op_sel_hi:[1,0]
	v_pk_mul_f32 v[8:9], v[8:9], v[2:3] op_sel_hi:[1,0]
	v_pk_mul_f32 v[12:13], v[12:13], v[2:3] op_sel_hi:[1,0]
	v_pk_mul_f32 v[36:37], v[36:37], v[2:3] op_sel_hi:[1,0]
	v_pk_mul_f32 v[0:1], v[0:1], v[2:3] op_sel_hi:[1,0]
	s_nop 0
	v_pk_fma_f32 v[6:7], v[206:207], v[4:5], v[222:223]
	v_pk_fma_f32 v[4:5], v[204:205], v[60:61], v[220:221]
	s_nop 1
	v_pk_mul_f32 v[60:61], v[10:11], v[2:3] op_sel_hi:[1,0]
	s_nop 0
	v_pk_fma_f32 v[10:11], v[210:211], v[8:9], v[226:227]
	v_pk_fma_f32 v[8:9], v[208:209], v[60:61], v[224:225]
	s_nop 1
	v_pk_mul_f32 v[60:61], v[14:15], v[2:3] op_sel_hi:[1,0]
	s_nop 0
	v_pk_fma_f32 v[14:15], v[214:215], v[12:13], v[230:231]
	v_pk_fma_f32 v[12:13], v[212:213], v[60:61], v[228:229]
	s_nop 1
	s_nop 0
	v_pk_fma_f32 v[18:19], v[0:1], v[218:219], v[234:235]
	v_pk_fma_f32 v[16:17], v[36:37], v[216:217], v[232:233]
	s_cbranch_vccnz .LBB0_1069
	v_add_co_u32_e32 v0, vcc, 0x2000, v34
	s_mov_b64 s[10:11], 0
	s_nop 0
	v_addc_co_u32_e32 v1, vcc, 0, v35, vcc
	global_store_dwordx4 v[0:1], v[4:7], off
	global_store_dwordx4 v[0:1], v[8:11], off offset:1024
	global_store_dwordx4 v[0:1], v[12:15], off offset:2048
	global_store_dwordx4 v[0:1], v[16:19], off offset:3072

; __device__ __forceinline__ void p7_combine(Frame& F, int l) {
;     ...
;         for (int r = 0; r < 4; ++r) {
; #pragma unroll
;             for (int j = 0; j < 4; ++j) { const int hw = (int)hv[r][j]; f32x4 a; a.x = (float)((hw << 24) >> 24) * hsa[r]; a.y = (float)((hw << 16) >> 24) * hsa[r]; a.z = (float)((hw << 8) >> 24) * hsa[r]; a.w = (float)(hw >> 24) * hsa[r];
;                 f32x4 ys = (f32x4){0.f, 0.f, 0.f, 0.f};
; #pragma unroll
;                 for (int k = 0; k < 4; ++k) { const int w = (int)yv[r][k][j]; ys.x += __builtin_amdgcn_cvt_f32_fp8(w, 0); ys.y += __builtin_amdgcn_cvt_f32_fp8(w, 1); ys.z += __builtin_amdgcn_cvt_f32_fp8(w, 2); ys.w += __builtin_amdgcn_cvt_f32_fp8(w, 3); }
;                 v[r][j] = a + ys * (1.0f / 16.0f); }
.LBB0_1073:
	s_waitcnt vmcnt(0)
	v_mul_f32_e32 v12, 0x3fb504f3, v3
	v_cvt_f32_fp8_e32 v0, v56
	v_cvt_f32_fp8_sdwa v1, v56 src0_sel:BYTE_1
	v_cvt_f32_fp8_sdwa v2, v56 src0_sel:BYTE_2
	v_cvt_f32_fp8_sdwa v3, v56 src0_sel:BYTE_3
	v_cvt_f32_fp8_e32 v4, v57
	v_cvt_f32_fp8_sdwa v5, v57 src0_sel:BYTE_1
	v_cvt_f32_fp8_sdwa v6, v57 src0_sel:BYTE_2
	v_cvt_f32_fp8_sdwa v7, v57 src0_sel:BYTE_3
	v_cvt_f32_fp8_e32 v8, v58
	v_cvt_f32_fp8_sdwa v9, v58 src0_sel:BYTE_1
	v_cvt_f32_fp8_sdwa v10, v58 src0_sel:BYTE_2
	v_cvt_f32_fp8_sdwa v11, v58 src0_sel:BYTE_3
	v_cvt_f32_fp8_e32 v14, v59
	v_cvt_f32_fp8_sdwa v15, v59 src0_sel:BYTE_1
	v_cvt_f32_fp8_sdwa v16, v59 src0_sel:BYTE_2
	v_cvt_f32_fp8_sdwa v17, v59 src0_sel:BYTE_3
	v_pk_add_f32 v[0:1], v[0:1], 0 op_sel_hi:[1,0]
	v_pk_add_f32 v[2:3], v[2:3], 0 op_sel_hi:[1,0]
	v_pk_add_f32 v[0:1], v[0:1], v[4:5]
	v_pk_add_f32 v[2:3], v[2:3], v[6:7]
	v_cvt_f32_i32_sdwa v5, sext(v43) dst_sel:DWORD dst_unused:UNUSED_PAD src0_sel:BYTE_3
	v_cvt_f32_i32_sdwa v7, sext(v43) dst_sel:DWORD dst_unused:UNUSED_PAD src0_sel:BYTE_1
	v_cvt_f32_i32_sdwa v6, sext(v43) dst_sel:DWORD dst_unused:UNUSED_PAD src0_sel:BYTE_0
	v_cvt_f32_i32_sdwa v4, sext(v43) dst_sel:DWORD dst_unused:UNUSED_PAD src0_sel:BYTE_2
	v_pk_add_f32 v[0:1], v[0:1], v[8:9]
	v_pk_add_f32 v[2:3], v[2:3], v[10:11]
	v_pk_add_f32 v[0:1], v[0:1], v[14:15]
	v_pk_add_f32 v[2:3], v[2:3], v[16:17]
	s_mov_b32 s10, 0x3d800000
	v_pk_mul_f32 v[8:9], v[0:1], s[10:11] op_sel_hi:[1,0]
	v_pk_mul_f32 v[0:1], v[2:3], s[10:11] op_sel_hi:[1,0]
	v_pk_fma_f32 v[2:3], v[12:13], v[6:7], v[8:9] op_sel_hi:[0,1,1]
	v_pk_fma_f32 v[0:1], v[12:13], v[4:5], v[0:1] op_sel_hi:[0,1,1]
	v_cvt_f32_fp8_e32 v4, v52
	v_cvt_f32_fp8_sdwa v5, v52 src0_sel:BYTE_1
	v_cvt_f32_fp8_sdwa v6, v52 src0_sel:BYTE_2
	v_cvt_f32_fp8_sdwa v7, v52 src0_sel:BYTE_3
	v_cvt_f32_fp8_e32 v8, v53
	v_cvt_f32_fp8_sdwa v9, v53 src0_sel:BYTE_1
	v_cvt_f32_fp8_sdwa v10, v53 src0_sel:BYTE_2
	v_cvt_f32_fp8_sdwa v11, v53 src0_sel:BYTE_3
	v_cvt_f32_fp8_e32 v14, v54
	v_cvt_f32_fp8_sdwa v15, v54 src0_sel:BYTE_1
	v_cvt_f32_fp8_sdwa v16, v54 src0_sel:BYTE_2
	v_cvt_f32_fp8_sdwa v17, v54 src0_sel:BYTE_3
	v_cvt_f32_fp8_e32 v18, v55
	v_cvt_f32_fp8_sdwa v19, v55 src0_sel:BYTE_1
	v_cvt_f32_fp8_sdwa v20, v55 src0_sel:BYTE_2
	v_cvt_f32_fp8_sdwa v21, v55 src0_sel:BYTE_3
	v_pk_add_f32 v[4:5], v[4:5], 0 op_sel_hi:[1,0]
	v_pk_add_f32 v[6:7], v[6:7], 0 op_sel_hi:[1,0]
	v_pk_add_f32 v[4:5], v[4:5], v[8:9]
	v_pk_add_f32 v[6:7], v[6:7], v[10:11]
	v_cvt_f32_i32_sdwa v9, sext(v42) dst_sel:DWORD dst_unused:UNUSED_PAD src0_sel:BYTE_3
	v_cvt_f32_i32_sdwa v11, sext(v42) dst_sel:DWORD dst_unused:UNUSED_PAD src0_sel:BYTE_1
	v_cvt_f32_i32_sdwa v10, sext(v42) dst_sel:DWORD dst_unused:UNUSED_PAD src0_sel:BYTE_0
	v_cvt_f32_i32_sdwa v8, sext(v42) dst_sel:DWORD dst_unused:UNUSED_PAD src0_sel:BYTE_2
	v_pk_add_f32 v[4:5], v[4:5], v[14:15]
	v_pk_add_f32 v[6:7], v[6:7], v[16:17]
	v_pk_add_f32 v[4:5], v[4:5], v[18:19]
	v_pk_add_f32 v[6:7], v[6:7], v[20:21]
	v_pk_mul_f32 v[14:15], v[4:5], s[10:11] op_sel_hi:[1,0]
	v_pk_mul_f32 v[4:5], v[6:7], s[10:11] op_sel_hi:[1,0]
	v_pk_fma_f32 v[6:7], v[12:13], v[10:11], v[14:15] op_sel_hi:[0,1,1]
	v_pk_fma_f32 v[4:5], v[12:13], v[8:9], v[4:5] op_sel_hi:[0,1,1]
	v_cvt_f32_fp8_e32 v8, v48
	v_cvt_f32_fp8_sdwa v9, v48 src0_sel:BYTE_1
	v_cvt_f32_fp8_sdwa v10, v48 src0_sel:BYTE_2
	v_cvt_f32_fp8_sdwa v11, v48 src0_sel:BYTE_3
	v_cvt_f32_fp8_e32 v14, v49
	v_cvt_f32_fp8_sdwa v15, v49 src0_sel:BYTE_1
	v_cvt_f32_fp8_sdwa v16, v49 src0_sel:BYTE_2
	v_cvt_f32_fp8_sdwa v17, v49 src0_sel:BYTE_3
	v_cvt_f32_fp8_e32 v18, v50
	v_cvt_f32_fp8_sdwa v19, v50 src0_sel:BYTE_1
	v_cvt_f32_fp8_sdwa v20, v50 src0_sel:BYTE_2
	v_cvt_f32_fp8_sdwa v21, v50 src0_sel:BYTE_3
	v_cvt_f32_fp8_e32 v22, v51
	v_cvt_f32_fp8_sdwa v23, v51 src0_sel:BYTE_1
	v_cvt_f32_fp8_sdwa v36, v51 src0_sel:BYTE_2
	v_cvt_f32_fp8_sdwa v37, v51 src0_sel:BYTE_3
	v_pk_add_f32 v[8:9], v[8:9], 0 op_sel_hi:[1,0]
	v_pk_add_f32 v[10:11], v[10:11], 0 op_sel_hi:[1,0]
	v_pk_add_f32 v[8:9], v[8:9], v[14:15]
	v_pk_add_f32 v[10:11], v[10:11], v[16:17]
	v_cvt_f32_i32_sdwa v15, sext(v41) dst_sel:DWORD dst_unused:UNUSED_PAD src0_sel:BYTE_3
	v_cvt_f32_i32_sdwa v14, sext(v41) dst_sel:DWORD dst_unused:UNUSED_PAD src0_sel:BYTE_2
	v_pk_add_f32 v[8:9], v[8:9], v[18:19]
	v_pk_add_f32 v[10:11], v[10:11], v[20:21]
	v_cvt_f32_i32_sdwa v17, sext(v41) dst_sel:DWORD dst_unused:UNUSED_PAD src0_sel:BYTE_1
	v_cvt_f32_i32_sdwa v16, sext(v41) dst_sel:DWORD dst_unused:UNUSED_PAD src0_sel:BYTE_0
	v_pk_add_f32 v[10:11], v[10:11], v[36:37]
	v_pk_add_f32 v[8:9], v[8:9], v[22:23]
	v_cvt_f32_fp8_sdwa v20, v45 src0_sel:BYTE_2
	v_pk_mul_f32 v[18:19], v[8:9], s[10:11] op_sel_hi:[1,0]
	v_pk_mul_f32 v[8:9], v[10:11], s[10:11] op_sel_hi:[1,0]
	v_pk_fma_f32 v[10:11], v[12:13], v[16:17], v[18:19] op_sel_hi:[0,1,1]
	v_pk_fma_f32 v[8:9], v[12:13], v[14:15], v[8:9] op_sel_hi:[0,1,1]
	v_cvt_f32_fp8_e32 v14, v44
	v_cvt_f32_fp8_sdwa v15, v44 src0_sel:BYTE_1
	v_cvt_f32_fp8_sdwa v16, v44 src0_sel:BYTE_2
	v_cvt_f32_fp8_sdwa v17, v44 src0_sel:BYTE_3
	v_cvt_f32_fp8_e32 v18, v45
	v_cvt_f32_fp8_sdwa v19, v45 src0_sel:BYTE_1
	v_cvt_f32_fp8_sdwa v21, v45 src0_sel:BYTE_3
	v_cvt_f32_fp8_e32 v22, v46
	v_cvt_f32_fp8_sdwa v23, v46 src0_sel:BYTE_1
	v_cvt_f32_fp8_sdwa v36, v46 src0_sel:BYTE_2
	v_cvt_f32_fp8_sdwa v37, v46 src0_sel:BYTE_3
	v_cvt_f32_fp8_e32 v42, v47
	v_cvt_f32_fp8_sdwa v43, v47 src0_sel:BYTE_1
	v_cvt_f32_fp8_sdwa v44, v47 src0_sel:BYTE_2
	v_cvt_f32_fp8_sdwa v45, v47 src0_sel:BYTE_3
	v_pk_add_f32 v[14:15], v[14:15], 0 op_sel_hi:[1,0]
	v_pk_add_f32 v[16:17], v[16:17], 0 op_sel_hi:[1,0]
	v_pk_add_f32 v[14:15], v[14:15], v[18:19]
	v_pk_add_f32 v[16:17], v[16:17], v[20:21]
; #define GAS __attribute__((address_space(1)))
; __device__ __forceinline__ void ln_row(f32x4 (&v)[4], const GAS float* g, const GAS float* b, int lane) {
;     float s = 0.f;
; #pragma unroll
;     for (int j = 0; j < 4; ++j) s += (v[j].x + v[j].y) + (v[j].z + v[j].w);
;     const float mean = wave_sum(s) * (1.f / D); float s2 = 0.f;
; #pragma unroll
;     for (int j = 0; j < 4; ++j) { v[j] = v[j] - mean; s2 += (v[j].x * v[j].x + v[j].y * v[j].y) + (v[j].z * v[j].z + v[j].w * v[j].w); }
;     const float rstd = __builtin_amdgcn_rsqf(wave_sum(s2) * (1.f / D) + LN_EPS);
; #pragma unroll
;     for (int j = 0; j < 4; ++j) { const f32x4 gg = *(const GAS f32x4*)(g + 4 * lane + 256 * j), bb = *(const GAS f32x4*)(b + 4 * lane + 256 * j); v[j] = v[j] * rstd * gg + bb; }
; }
; __device__ __forceinline__ void p7_combine(Frame& F, int l) {
;     ...
;             ln_row(v[r], g2, b2, lane);
;             if (lastl) store_row_f(v[r], F.H + (size_t)(m + r) * D, lane);
;             else store_row_q(v[r], HQ + (size_t)(m + r) * D, HS + m + r, lane); }
	v_pk_add_f32 v[14:15], v[14:15], v[22:23]
	v_cvt_f32_i32_sdwa v19, sext(v40) dst_sel:DWORD dst_unused:UNUSED_PAD src0_sel:BYTE_3
	v_cvt_f32_i32_sdwa v23, sext(v40) dst_sel:DWORD dst_unused:UNUSED_PAD src0_sel:BYTE_1
	v_cvt_f32_i32_sdwa v22, sext(v40) dst_sel:DWORD dst_unused:UNUSED_PAD src0_sel:BYTE_0
	v_cvt_f32_i32_sdwa v18, sext(v40) dst_sel:DWORD dst_unused:UNUSED_PAD src0_sel:BYTE_2
	v_pk_add_f32 v[16:17], v[16:17], v[36:37]
	v_pk_add_f32 v[14:15], v[14:15], v[42:43]
	v_pk_add_f32 v[16:17], v[16:17], v[44:45]
	v_pk_mul_f32 v[14:15], v[14:15], s[10:11] op_sel_hi:[1,0]
	v_pk_mul_f32 v[16:17], v[16:17], s[10:11] op_sel_hi:[1,0]
	v_pk_fma_f32 v[22:23], v[12:13], v[22:23], v[14:15] op_sel_hi:[0,1,1]
	v_pk_fma_f32 v[20:21], v[12:13], v[18:19], v[16:17] op_sel_hi:[0,1,1]
	v_pk_mov_b32 v[12:13], v[2:3], v[0:1] op_sel:[1,0]
	v_mov_b32_e32 v14, v2
	v_mov_b32_e32 v15, v1
	v_pk_add_f32 v[12:13], v[12:13], v[14:15]
	v_pk_mov_b32 v[14:15], v[6:7], v[4:5] op_sel:[1,0]
	v_mov_b32_e32 v16, v6
	v_mov_b32_e32 v17, v5
	v_pk_add_f32 v[14:15], v[14:15], v[16:17]
	v_add_f32_e32 v12, v12, v13
	v_pk_add_f32 v[14:15], v[14:15], v[14:15] op_sel:[0,1] op_sel_hi:[1,0]
	v_add_f32_e32 v12, 0, v12
	v_add_f32_e32 v16, v10, v11
	v_add_f32_e32 v18, v8, v9
	v_mov_b32_e32 v13, v22
	v_mov_b32_e32 v15, v23
	v_mov_b32_e32 v17, v20
	v_mov_b32_e32 v19, v21
	v_pk_add_f32 v[12:13], v[12:13], v[14:15]
	v_pk_add_f32 v[14:15], v[16:17], v[18:19]
	s_and_b64 vcc, exec, s[36:37]
	v_pk_add_f32 v[12:13], v[12:13], v[14:15]
	s_nop 0
	v_add_f32_e32 v12, v12, v13
	v_mov_b32_e32 v13, v12
	s_nop 1
	v_mov_b32_dpp v13, v13 quad_perm:[1,0,3,2] row_mask:0xf bank_mask:0xf
	v_add_f32_e32 v12, v12, v13
	v_mov_b32_e32 v13, v12
	s_nop 1
	v_mov_b32_dpp v13, v13 quad_perm:[2,3,0,1] row_mask:0xf bank_mask:0xf
	v_add_f32_e32 v12, v12, v13
	v_mov_b32_e32 v13, v12
	s_nop 1
	v_mov_b32_dpp v13, v13 row_ror:4 row_mask:0xf bank_mask:0xf
	v_add_f32_e32 v12, v12, v13
	v_mov_b32_e32 v13, v12
	s_nop 1
	v_mov_b32_dpp v13, v13 row_ror:8 row_mask:0xf bank_mask:0xf
	v_add_f32_e32 v12, v12, v13
	v_mov_b32_e32 v13, v12
	s_nop 1
	v_mov_b32_dpp v13, v13 row_bcast:15 row_mask:0xa bank_mask:0xf
	v_add_f32_e32 v12, v12, v13
	v_mov_b32_e32 v13, v12
	s_nop 1
	v_mov_b32_dpp v13, v13 row_bcast:31 row_mask:0xc bank_mask:0xf
	v_add_f32_e32 v12, v12, v13
	s_nop 0
	v_readlane_b32 s10, v12, 63
	s_nop 1
	v_fma_f32 v3, s10, v196, v3
	v_fmac_f32_e32 v2, s10, v196
	v_fma_f32 v1, s10, v196, v1
	v_fmac_f32_e32 v0, s10, v196
	v_pk_mul_f32 v[12:13], v[0:1], v[0:1]
	v_pk_mul_f32 v[14:15], v[2:3], v[2:3]
	v_fma_f32 v7, s10, v196, v7
	v_pk_mov_b32 v[16:17], v[14:15], v[12:13] op_sel:[1,0]
	v_mov_b32_e32 v15, v13
	v_pk_add_f32 v[12:13], v[16:17], v[14:15]
	v_fmac_f32_e32 v6, s10, v196
	v_fma_f32 v5, s10, v196, v5
	v_fmac_f32_e32 v4, s10, v196
	v_pk_add_f32 v[12:13], v[12:13], v[12:13] op_sel_hi:[0,1]
	v_pk_mul_f32 v[14:15], v[4:5], v[4:5]
	v_pk_mul_f32 v[16:17], v[6:7], v[6:7]
	v_fmac_f32_e32 v10, s10, v196
	v_pk_mov_b32 v[18:19], v[16:17], v[14:15] op_sel:[1,0]
	v_mov_b32_e32 v17, v15
	v_fma_f32 v11, s10, v196, v11
	v_fmac_f32_e32 v8, s10, v196
	v_mul_f32_e32 v12, v10, v10
	v_pk_add_f32 v[14:15], v[18:19], v[16:17]
	v_fma_f32 v9, s10, v196, v9
	v_pk_fma_f32 v[16:17], v[10:11], v[10:11], v[12:13] op_sel_hi:[1,1,0]
	v_mul_f32_e32 v12, v8, v8
	v_pk_add_f32 v[14:15], v[14:15], v[14:15] op_sel_hi:[0,1]
	v_pk_fma_f32 v[18:19], v[8:9], v[8:9], v[12:13] op_sel_hi:[1,1,0]
	v_fma_f32 v21, s10, v196, v21
	v_fmac_f32_e32 v20, s10, v196
	v_fma_f32 v23, s10, v196, v23
	v_fmac_f32_e32 v22, s10, v196
	v_mul_f32_e32 v16, v22, v22
	v_mul_f32_e32 v18, v23, v23
	v_mul_f32_e32 v12, v20, v20
	v_mul_f32_e32 v14, v21, v21
	v_pk_add_f32 v[16:17], v[16:17], v[18:19]
	v_pk_add_f32 v[12:13], v[12:13], v[14:15]
	s_nop 0
	v_pk_add_f32 v[12:13], v[16:17], v[12:13]
	s_nop 0
	v_add_f32_e32 v12, v12, v13
	v_mov_b32_e32 v13, v12
	s_nop 1
	v_mov_b32_dpp v13, v13 quad_perm:[1,0,3,2] row_mask:0xf bank_mask:0xf
	v_add_f32_e32 v12, v12, v13
	v_mov_b32_e32 v13, v12
	s_nop 1
	v_mov_b32_dpp v13, v13 quad_perm:[2,3,0,1] row_mask:0xf bank_mask:0xf
	v_add_f32_e32 v12, v12, v13
	v_mov_b32_e32 v13, v12
	s_nop 1
	v_mov_b32_dpp v13, v13 row_ror:4 row_mask:0xf bank_mask:0xf
	v_add_f32_e32 v12, v12, v13
	v_mov_b32_e32 v13, v12
	s_nop 1
	v_mov_b32_dpp v13, v13 row_ror:8 row_mask:0xf bank_mask:0xf
	v_add_f32_e32 v12, v12, v13
	v_mov_b32_e32 v13, v12
	s_nop 1
	v_mov_b32_dpp v13, v13 row_bcast:15 row_mask:0xa bank_mask:0xf
	v_add_f32_e32 v12, v12, v13
	v_mov_b32_e32 v13, v12
	s_nop 1
	v_mov_b32_dpp v13, v13 row_bcast:31 row_mask:0xc bank_mask:0xf
	v_add_f32_e32 v12, v12, v13
	s_nop 0
	v_readlane_b32 s10, v12, 63
	s_nop 1
	v_fma_f32 v12, s10, v197, v190
	v_rsq_f32_e32 v36, v12
	s_nop 1
	s_mov_b64 s[10:11], -1
	v_pk_mul_f32 v[40:41], v[2:3], v[36:37] op_sel_hi:[1,0]
	v_pk_mul_f32 v[0:1], v[0:1], v[36:37] op_sel_hi:[1,0]
	v_pk_mul_f32 v[4:5], v[4:5], v[36:37] op_sel_hi:[1,0]
	v_pk_mul_f32 v[8:9], v[8:9], v[36:37] op_sel_hi:[1,0]
	v_pk_mul_f32 v[22:23], v[22:23], v[36:37] op_sel_hi:[1,0]
	v_pk_mul_f32 v[20:21], v[20:21], v[36:37] op_sel_hi:[1,0]
	s_nop 0
	v_pk_fma_f32 v[2:3], v[206:207], v[0:1], v[222:223]
	v_pk_fma_f32 v[0:1], v[204:205], v[40:41], v[220:221]
	s_nop 1
	v_pk_mul_f32 v[40:41], v[6:7], v[36:37] op_sel_hi:[1,0]
	s_nop 0
	v_pk_fma_f32 v[6:7], v[210:211], v[4:5], v[226:227]
	v_pk_fma_f32 v[4:5], v[208:209], v[40:41], v[224:225]
	s_nop 1
	v_pk_mul_f32 v[40:41], v[10:11], v[36:37] op_sel_hi:[1,0]
	s_nop 0
	v_pk_fma_f32 v[10:11], v[214:215], v[8:9], v[230:231]
	v_pk_fma_f32 v[8:9], v[212:213], v[40:41], v[228:229]
	s_nop 1
	s_nop 0
	v_pk_fma_f32 v[14:15], v[20:21], v[218:219], v[234:235]
	v_pk_fma_f32 v[12:13], v[22:23], v[216:217], v[232:233]
	s_cbranch_vccnz .LBB0_1075
	v_add_co_u32_e32 v16, vcc, 0x3000, v34
	s_mov_b64 s[10:11], 0
	s_nop 0
	v_addc_co_u32_e32 v17, vcc, 0, v35, vcc
	global_store_dwordx4 v[16:17], v[0:3], off
	global_store_dwordx4 v[16:17], v[4:7], off offset:1024
	global_store_dwordx4 v[16:17], v[8:11], off offset:2048
	global_store_dwordx4 v[16:17], v[12:15], off offset:3072
